# merge GEMM epilogue rewritten by hand: all gate loads issued up front with counted waits; the raw next-branch gate words of six of sixteen positions stay in spare VGPRs for the next unit (fewer gate r
# speedup vs baseline: 1.0124x; 1.0026x over previous
.LBB0_1217:
	s_ashr_i32 s30, s63, 2
	s_lshl_b32 s4, s30, 15
	s_lshl_b32 s5, s67, 8
	s_sub_i32 s4, s5, s4
	v_add_u32_e32 v2, s4, v165
	s_lshl_b32 s5, s63, 8
	s_and_b32 s5, s5, 0x300
	v_add_u32_e32 v0, s5, v189
	v_mul_u32_u24_e32 v191, 0x1800, v2
	v_lshl_add_u32 v191, v0, 1, v191
	v_lshlrev_b32_e32 v3, 11, v2
	v_lshl_add_u32 v3, v0, 1, v3
	s_lshl_b32 s26, s30, 11
	s_add_u32 s26, s14, s26
	s_addc_u32 s27, s15, 0
	s_cmp_eq_u32 s30, 2
	s_cbranch_scc1 .Lmg_last
	s_cmp_eq_u32 s30, 1
	s_cbranch_scc1 .Lmg_mid
	s_add_u32 s28, s26, 0x0
	s_addc_u32 s29, s27, 0
	global_load_dwordx4 v[132:135], v191, s[28:29]
	global_load_dwordx4 v[136:139], v191, s[28:29] offset:2048
	s_add_u32 s28, s26, 0x0
	s_addc_u32 s29, s27, 0
	global_load_dwordx4 v[140:143], v191, s[28:29] offset:256
	global_load_dwordx4 v[144:147], v191, s[28:29] offset:2304
	s_add_u32 s28, s26, 0x18000
	s_addc_u32 s29, s27, 0
	global_load_dwordx4 v[148:151], v191, s[28:29]
	global_load_dwordx4 v[152:155], v191, s[28:29] offset:2048
	s_add_u32 s28, s26, 0x18000
	s_addc_u32 s29, s27, 0
	global_load_dwordx4 v[156:159], v191, s[28:29] offset:256
	global_load_dwordx4 v[160:163], v191, s[28:29] offset:2304
	s_add_u32 s28, s26, 0x30000
	s_addc_u32 s29, s27, 0
	global_load_dwordx4 v[180:183], v191, s[28:29]
	global_load_dwordx4 v[184:187], v191, s[28:29] offset:2048
	s_add_u32 s28, s26, 0x30000
	s_addc_u32 s29, s27, 0
	global_load_dwordx4 v[192:195], v191, s[28:29] offset:256
	global_load_dwordx4 v[196:199], v191, s[28:29] offset:2304
	s_add_u32 s28, s26, 0x48000
	s_addc_u32 s29, s27, 0
	global_load_dwordx4 v[212:215], v191, s[28:29]
	global_load_dwordx4 v[216:219], v191, s[28:29] offset:2048
	s_and_b64 vcc, exec, s[20:21]
	s_cbranch_vccz .Lmg_nba
	s_barrier
.Lmg_nba:
	s_waitcnt vmcnt(12)
	v_lshlrev_b32_e32 v168, 16, v132
	v_and_b32_e32 v169, 0xffff0000, v132
	v_lshlrev_b32_e32 v170, 16, v133
	v_and_b32_e32 v171, 0xffff0000, v133
	v_lshlrev_b32_e32 v224, 16, v134
	v_and_b32_e32 v225, 0xffff0000, v134
	v_lshlrev_b32_e32 v226, 16, v135
	v_and_b32_e32 v227, 0xffff0000, v135
	v_max_f32_e32 v168, 0x1e3ce508, v168
	v_max_f32_e32 v169, 0x1e3ce508, v169
	v_max_f32_e32 v170, 0x1e3ce508, v170
	v_max_f32_e32 v171, 0x1e3ce508, v171
	v_max_f32_e32 v224, 0x1e3ce508, v224
	v_max_f32_e32 v225, 0x1e3ce508, v225
	v_max_f32_e32 v226, 0x1e3ce508, v226
	v_max_f32_e32 v227, 0x1e3ce508, v227
	v_mov_b32_e32 v228, v136
	v_mov_b32_e32 v229, v137
	v_mov_b32_e32 v230, v138
	v_mov_b32_e32 v231, v139
	v_lshlrev_b32_e32 v132, 16, v136
	v_and_b32_e32 v133, 0xffff0000, v136
	v_lshlrev_b32_e32 v134, 16, v137
	v_and_b32_e32 v135, 0xffff0000, v137
	v_lshlrev_b32_e32 v136, 16, v138
	v_and_b32_e32 v137, 0xffff0000, v138
	v_lshlrev_b32_e32 v138, 16, v139
	v_and_b32_e32 v139, 0xffff0000, v139
	v_max_f32_e32 v132, 0x1e3ce508, v132
	v_max_f32_e32 v133, 0x1e3ce508, v133
	v_max_f32_e32 v134, 0x1e3ce508, v134
	v_max_f32_e32 v135, 0x1e3ce508, v135
	v_max_f32_e32 v136, 0x1e3ce508, v136
	v_max_f32_e32 v137, 0x1e3ce508, v137
	v_max_f32_e32 v138, 0x1e3ce508, v138
	v_max_f32_e32 v139, 0x1e3ce508, v139
	v_rcp_f32_e32 v132, v132
	v_rcp_f32_e32 v133, v133
	v_rcp_f32_e32 v134, v134
	v_rcp_f32_e32 v135, v135
	v_rcp_f32_e32 v136, v136
	v_rcp_f32_e32 v137, v137
	v_rcp_f32_e32 v138, v138
	v_rcp_f32_e32 v139, v139
	v_pk_mul_f32 v[168:169], v[168:169], v[132:133]
	v_pk_mul_f32 v[170:171], v[170:171], v[134:135]
	v_pk_mul_f32 v[224:225], v[224:225], v[136:137]
	v_pk_mul_f32 v[226:227], v[226:227], v[138:139]
	v_pk_mul_f32 v[112:113], v[112:113], v[168:169]
	v_pk_mul_f32 v[114:115], v[114:115], v[170:171]
	v_pk_mul_f32 v[108:109], v[108:109], v[224:225]
	v_pk_mul_f32 v[110:111], v[110:111], v[226:227]
	s_add_u32 s28, s26, 0x48000
	s_addc_u32 s29, s27, 0
	global_load_dwordx4 v[220:223], v191, s[28:29] offset:256
	global_load_dwordx4 v[132:135], v191, s[28:29] offset:2304
	s_waitcnt vmcnt(12)
	v_lshlrev_b32_e32 v168, 16, v140
	v_and_b32_e32 v169, 0xffff0000, v140
	v_lshlrev_b32_e32 v170, 16, v141
	v_and_b32_e32 v171, 0xffff0000, v141
	v_lshlrev_b32_e32 v224, 16, v142
	v_and_b32_e32 v225, 0xffff0000, v142
	v_lshlrev_b32_e32 v226, 16, v143
	v_and_b32_e32 v227, 0xffff0000, v143
	v_max_f32_e32 v168, 0x1e3ce508, v168
	v_max_f32_e32 v169, 0x1e3ce508, v169
	v_max_f32_e32 v170, 0x1e3ce508, v170
	v_max_f32_e32 v171, 0x1e3ce508, v171
	v_max_f32_e32 v224, 0x1e3ce508, v224
	v_max_f32_e32 v225, 0x1e3ce508, v225
	v_max_f32_e32 v226, 0x1e3ce508, v226
	v_max_f32_e32 v227, 0x1e3ce508, v227
	v_mov_b32_e32 v232, v144
	v_mov_b32_e32 v233, v145
	v_mov_b32_e32 v234, v146
	v_mov_b32_e32 v235, v147
	v_lshlrev_b32_e32 v140, 16, v144
	v_and_b32_e32 v141, 0xffff0000, v144
	v_lshlrev_b32_e32 v142, 16, v145
	v_and_b32_e32 v143, 0xffff0000, v145
	v_lshlrev_b32_e32 v144, 16, v146
	v_and_b32_e32 v145, 0xffff0000, v146
	v_lshlrev_b32_e32 v146, 16, v147
	v_and_b32_e32 v147, 0xffff0000, v147
	v_max_f32_e32 v140, 0x1e3ce508, v140
	v_max_f32_e32 v141, 0x1e3ce508, v141
	v_max_f32_e32 v142, 0x1e3ce508, v142
	v_max_f32_e32 v143, 0x1e3ce508, v143
	v_max_f32_e32 v144, 0x1e3ce508, v144
	v_max_f32_e32 v145, 0x1e3ce508, v145
	v_max_f32_e32 v146, 0x1e3ce508, v146
	v_max_f32_e32 v147, 0x1e3ce508, v147
	v_rcp_f32_e32 v140, v140
	v_rcp_f32_e32 v141, v141
	v_rcp_f32_e32 v142, v142
	v_rcp_f32_e32 v143, v143
	v_rcp_f32_e32 v144, v144
	v_rcp_f32_e32 v145, v145
	v_rcp_f32_e32 v146, v146
	v_rcp_f32_e32 v147, v147
	v_pk_mul_f32 v[168:169], v[168:169], v[140:141]
	v_pk_mul_f32 v[170:171], v[170:171], v[142:143]
	v_pk_mul_f32 v[224:225], v[224:225], v[144:145]
	v_pk_mul_f32 v[226:227], v[226:227], v[146:147]
	v_pk_mul_f32 v[80:81], v[80:81], v[168:169]
	v_pk_mul_f32 v[82:83], v[82:83], v[170:171]
	v_pk_mul_f32 v[76:77], v[76:77], v[224:225]
	v_pk_mul_f32 v[78:79], v[78:79], v[226:227]
	s_add_u32 s28, s26, 0xc0000
	s_addc_u32 s29, s27, 0
	global_load_dwordx4 v[136:139], v191, s[28:29]
	global_load_dwordx4 v[140:143], v191, s[28:29] offset:2048
	s_waitcnt vmcnt(12)
	v_lshlrev_b32_e32 v168, 16, v148
	v_and_b32_e32 v169, 0xffff0000, v148
	v_lshlrev_b32_e32 v170, 16, v149
	v_and_b32_e32 v171, 0xffff0000, v149
	v_lshlrev_b32_e32 v224, 16, v150
	v_and_b32_e32 v225, 0xffff0000, v150
	v_lshlrev_b32_e32 v226, 16, v151
	v_and_b32_e32 v227, 0xffff0000, v151
	v_max_f32_e32 v168, 0x1e3ce508, v168
	v_max_f32_e32 v169, 0x1e3ce508, v169
	v_max_f32_e32 v170, 0x1e3ce508, v170
	v_max_f32_e32 v171, 0x1e3ce508, v171
	v_max_f32_e32 v224, 0x1e3ce508, v224
	v_max_f32_e32 v225, 0x1e3ce508, v225
	v_max_f32_e32 v226, 0x1e3ce508, v226
	v_max_f32_e32 v227, 0x1e3ce508, v227
	v_mov_b32_e32 v236, v152
	v_mov_b32_e32 v237, v153
	v_mov_b32_e32 v238, v154
	v_mov_b32_e32 v239, v155
	v_lshlrev_b32_e32 v148, 16, v152
	v_and_b32_e32 v149, 0xffff0000, v152
	v_lshlrev_b32_e32 v150, 16, v153
	v_and_b32_e32 v151, 0xffff0000, v153
	v_lshlrev_b32_e32 v152, 16, v154
	v_and_b32_e32 v153, 0xffff0000, v154
	v_lshlrev_b32_e32 v154, 16, v155
	v_and_b32_e32 v155, 0xffff0000, v155
	v_max_f32_e32 v148, 0x1e3ce508, v148
	v_max_f32_e32 v149, 0x1e3ce508, v149
	v_max_f32_e32 v150, 0x1e3ce508, v150
	v_max_f32_e32 v151, 0x1e3ce508, v151
	v_max_f32_e32 v152, 0x1e3ce508, v152
	v_max_f32_e32 v153, 0x1e3ce508, v153
	v_max_f32_e32 v154, 0x1e3ce508, v154
	v_max_f32_e32 v155, 0x1e3ce508, v155
	v_rcp_f32_e32 v148, v148
	v_rcp_f32_e32 v149, v149
	v_rcp_f32_e32 v150, v150
	v_rcp_f32_e32 v151, v151
	v_rcp_f32_e32 v152, v152
	v_rcp_f32_e32 v153, v153
	v_rcp_f32_e32 v154, v154
	v_rcp_f32_e32 v155, v155
	v_pk_mul_f32 v[168:169], v[168:169], v[148:149]
	v_pk_mul_f32 v[170:171], v[170:171], v[150:151]
	v_pk_mul_f32 v[224:225], v[224:225], v[152:153]
	v_pk_mul_f32 v[226:227], v[226:227], v[154:155]
	v_pk_mul_f32 v[104:105], v[104:105], v[168:169]
	v_pk_mul_f32 v[106:107], v[106:107], v[170:171]
	v_pk_mul_f32 v[100:101], v[100:101], v[224:225]
	v_pk_mul_f32 v[102:103], v[102:103], v[226:227]
	s_add_u32 s28, s26, 0xc0000
	s_addc_u32 s29, s27, 0
	global_load_dwordx4 v[144:147], v191, s[28:29] offset:256
	global_load_dwordx4 v[148:151], v191, s[28:29] offset:2304
	s_waitcnt vmcnt(12)
	v_lshlrev_b32_e32 v168, 16, v156
	v_and_b32_e32 v169, 0xffff0000, v156
	v_lshlrev_b32_e32 v170, 16, v157
	v_and_b32_e32 v171, 0xffff0000, v157
	v_lshlrev_b32_e32 v224, 16, v158
	v_and_b32_e32 v225, 0xffff0000, v158
	v_lshlrev_b32_e32 v226, 16, v159
	v_and_b32_e32 v227, 0xffff0000, v159
	v_max_f32_e32 v168, 0x1e3ce508, v168
	v_max_f32_e32 v169, 0x1e3ce508, v169
	v_max_f32_e32 v170, 0x1e3ce508, v170
	v_max_f32_e32 v171, 0x1e3ce508, v171
	v_max_f32_e32 v224, 0x1e3ce508, v224
	v_max_f32_e32 v225, 0x1e3ce508, v225
	v_max_f32_e32 v226, 0x1e3ce508, v226
	v_max_f32_e32 v227, 0x1e3ce508, v227
	v_mov_b32_e32 v240, v160
	v_mov_b32_e32 v241, v161
	v_mov_b32_e32 v242, v162
	v_mov_b32_e32 v243, v163
	v_lshlrev_b32_e32 v156, 16, v160
	v_and_b32_e32 v157, 0xffff0000, v160
	v_lshlrev_b32_e32 v158, 16, v161
	v_and_b32_e32 v159, 0xffff0000, v161
	v_lshlrev_b32_e32 v160, 16, v162
	v_and_b32_e32 v161, 0xffff0000, v162
	v_lshlrev_b32_e32 v162, 16, v163
	v_and_b32_e32 v163, 0xffff0000, v163
	v_max_f32_e32 v156, 0x1e3ce508, v156
	v_max_f32_e32 v157, 0x1e3ce508, v157
	v_max_f32_e32 v158, 0x1e3ce508, v158
	v_max_f32_e32 v159, 0x1e3ce508, v159
	v_max_f32_e32 v160, 0x1e3ce508, v160
	v_max_f32_e32 v161, 0x1e3ce508, v161
	v_max_f32_e32 v162, 0x1e3ce508, v162
	v_max_f32_e32 v163, 0x1e3ce508, v163
	v_rcp_f32_e32 v156, v156
	v_rcp_f32_e32 v157, v157
	v_rcp_f32_e32 v158, v158
	v_rcp_f32_e32 v159, v159
	v_rcp_f32_e32 v160, v160
	v_rcp_f32_e32 v161, v161
	v_rcp_f32_e32 v162, v162
	v_rcp_f32_e32 v163, v163
	v_pk_mul_f32 v[168:169], v[168:169], v[156:157]
	v_pk_mul_f32 v[170:171], v[170:171], v[158:159]
	v_pk_mul_f32 v[224:225], v[224:225], v[160:161]
	v_pk_mul_f32 v[226:227], v[226:227], v[162:163]
	v_pk_mul_f32 v[72:73], v[72:73], v[168:169]
	v_pk_mul_f32 v[74:75], v[74:75], v[170:171]
	v_pk_mul_f32 v[68:69], v[68:69], v[224:225]
	v_pk_mul_f32 v[70:71], v[70:71], v[226:227]
	s_add_u32 s28, s26, 0xd8000
	s_addc_u32 s29, s27, 0
	global_load_dwordx4 v[152:155], v191, s[28:29]
	global_load_dwordx4 v[156:159], v191, s[28:29] offset:2048
	s_waitcnt vmcnt(12)
	v_lshlrev_b32_e32 v168, 16, v180
	v_and_b32_e32 v169, 0xffff0000, v180
	v_lshlrev_b32_e32 v170, 16, v181
	v_and_b32_e32 v171, 0xffff0000, v181
	v_lshlrev_b32_e32 v224, 16, v182
	v_and_b32_e32 v225, 0xffff0000, v182
	v_lshlrev_b32_e32 v226, 16, v183
	v_and_b32_e32 v227, 0xffff0000, v183
	v_max_f32_e32 v168, 0x1e3ce508, v168
	v_max_f32_e32 v169, 0x1e3ce508, v169
	v_max_f32_e32 v170, 0x1e3ce508, v170
	v_max_f32_e32 v171, 0x1e3ce508, v171
	v_max_f32_e32 v224, 0x1e3ce508, v224
	v_max_f32_e32 v225, 0x1e3ce508, v225
	v_max_f32_e32 v226, 0x1e3ce508, v226
	v_max_f32_e32 v227, 0x1e3ce508, v227
	v_mov_b32_e32 v244, v184
	v_mov_b32_e32 v245, v185
	v_mov_b32_e32 v246, v186
	v_mov_b32_e32 v247, v187
	v_lshlrev_b32_e32 v180, 16, v184
	v_and_b32_e32 v181, 0xffff0000, v184
	v_lshlrev_b32_e32 v182, 16, v185
	v_and_b32_e32 v183, 0xffff0000, v185
	v_lshlrev_b32_e32 v184, 16, v186
	v_and_b32_e32 v185, 0xffff0000, v186
	v_lshlrev_b32_e32 v186, 16, v187
	v_and_b32_e32 v187, 0xffff0000, v187
	v_max_f32_e32 v180, 0x1e3ce508, v180
	v_max_f32_e32 v181, 0x1e3ce508, v181
	v_max_f32_e32 v182, 0x1e3ce508, v182
	v_max_f32_e32 v183, 0x1e3ce508, v183
	v_max_f32_e32 v184, 0x1e3ce508, v184
	v_max_f32_e32 v185, 0x1e3ce508, v185
	v_max_f32_e32 v186, 0x1e3ce508, v186
	v_max_f32_e32 v187, 0x1e3ce508, v187
	v_rcp_f32_e32 v180, v180
	v_rcp_f32_e32 v181, v181
	v_rcp_f32_e32 v182, v182
	v_rcp_f32_e32 v183, v183
	v_rcp_f32_e32 v184, v184
	v_rcp_f32_e32 v185, v185
	v_rcp_f32_e32 v186, v186
	v_rcp_f32_e32 v187, v187
	v_pk_mul_f32 v[168:169], v[168:169], v[180:181]
	v_pk_mul_f32 v[170:171], v[170:171], v[182:183]
	v_pk_mul_f32 v[224:225], v[224:225], v[184:185]
	v_pk_mul_f32 v[226:227], v[226:227], v[186:187]
	v_pk_mul_f32 v[96:97], v[96:97], v[168:169]
	v_pk_mul_f32 v[98:99], v[98:99], v[170:171]
	v_pk_mul_f32 v[92:93], v[92:93], v[224:225]
	v_pk_mul_f32 v[94:95], v[94:95], v[226:227]
	s_add_u32 s28, s26, 0xd8000
	s_addc_u32 s29, s27, 0
	global_load_dwordx4 v[160:163], v191, s[28:29] offset:256
	global_load_dwordx4 v[180:183], v191, s[28:29] offset:2304
	s_waitcnt vmcnt(12)
	v_lshlrev_b32_e32 v168, 16, v192
	v_and_b32_e32 v169, 0xffff0000, v192
	v_lshlrev_b32_e32 v170, 16, v193
	v_and_b32_e32 v171, 0xffff0000, v193
	v_lshlrev_b32_e32 v224, 16, v194
	v_and_b32_e32 v225, 0xffff0000, v194
	v_lshlrev_b32_e32 v226, 16, v195
	v_and_b32_e32 v227, 0xffff0000, v195
	v_max_f32_e32 v168, 0x1e3ce508, v168
	v_max_f32_e32 v169, 0x1e3ce508, v169
	v_max_f32_e32 v170, 0x1e3ce508, v170
	v_max_f32_e32 v171, 0x1e3ce508, v171
	v_max_f32_e32 v224, 0x1e3ce508, v224
	v_max_f32_e32 v225, 0x1e3ce508, v225
	v_max_f32_e32 v226, 0x1e3ce508, v226
	v_max_f32_e32 v227, 0x1e3ce508, v227
	v_mov_b32_e32 v248, v196
	v_mov_b32_e32 v249, v197
	v_mov_b32_e32 v250, v198
	v_mov_b32_e32 v251, v199
	v_lshlrev_b32_e32 v192, 16, v196
	v_and_b32_e32 v193, 0xffff0000, v196
	v_lshlrev_b32_e32 v194, 16, v197
	v_and_b32_e32 v195, 0xffff0000, v197
	v_lshlrev_b32_e32 v196, 16, v198
	v_and_b32_e32 v197, 0xffff0000, v198
	v_lshlrev_b32_e32 v198, 16, v199
	v_and_b32_e32 v199, 0xffff0000, v199
	v_max_f32_e32 v192, 0x1e3ce508, v192
	v_max_f32_e32 v193, 0x1e3ce508, v193
	v_max_f32_e32 v194, 0x1e3ce508, v194
	v_max_f32_e32 v195, 0x1e3ce508, v195
	v_max_f32_e32 v196, 0x1e3ce508, v196
	v_max_f32_e32 v197, 0x1e3ce508, v197
	v_max_f32_e32 v198, 0x1e3ce508, v198
	v_max_f32_e32 v199, 0x1e3ce508, v199
	v_rcp_f32_e32 v192, v192
	v_rcp_f32_e32 v193, v193
	v_rcp_f32_e32 v194, v194
	v_rcp_f32_e32 v195, v195
	v_rcp_f32_e32 v196, v196
	v_rcp_f32_e32 v197, v197
	v_rcp_f32_e32 v198, v198
	v_rcp_f32_e32 v199, v199
	v_pk_mul_f32 v[168:169], v[168:169], v[192:193]
	v_pk_mul_f32 v[170:171], v[170:171], v[194:195]
	v_pk_mul_f32 v[224:225], v[224:225], v[196:197]
	v_pk_mul_f32 v[226:227], v[226:227], v[198:199]
	v_pk_mul_f32 v[64:65], v[64:65], v[168:169]
	v_pk_mul_f32 v[66:67], v[66:67], v[170:171]
	v_pk_mul_f32 v[60:61], v[60:61], v[224:225]
	v_pk_mul_f32 v[62:63], v[62:63], v[226:227]
	s_add_u32 s28, s26, 0xf0000
	s_addc_u32 s29, s27, 0
	global_load_dwordx4 v[184:187], v191, s[28:29]
	global_load_dwordx4 v[192:195], v191, s[28:29] offset:2048
	s_waitcnt vmcnt(12)
	v_lshlrev_b32_e32 v168, 16, v212
	v_and_b32_e32 v169, 0xffff0000, v212
	v_lshlrev_b32_e32 v170, 16, v213
	v_and_b32_e32 v171, 0xffff0000, v213
	v_lshlrev_b32_e32 v224, 16, v214
	v_and_b32_e32 v225, 0xffff0000, v214
	v_lshlrev_b32_e32 v226, 16, v215
	v_and_b32_e32 v227, 0xffff0000, v215
	v_max_f32_e32 v168, 0x1e3ce508, v168
	v_max_f32_e32 v169, 0x1e3ce508, v169
	v_max_f32_e32 v170, 0x1e3ce508, v170
	v_max_f32_e32 v171, 0x1e3ce508, v171
	v_max_f32_e32 v224, 0x1e3ce508, v224
	v_max_f32_e32 v225, 0x1e3ce508, v225
	v_max_f32_e32 v226, 0x1e3ce508, v226
	v_max_f32_e32 v227, 0x1e3ce508, v227
	v_lshlrev_b32_e32 v212, 16, v216
	v_and_b32_e32 v213, 0xffff0000, v216
	v_lshlrev_b32_e32 v214, 16, v217
	v_and_b32_e32 v215, 0xffff0000, v217
	v_lshlrev_b32_e32 v216, 16, v218
	v_and_b32_e32 v217, 0xffff0000, v218
	v_lshlrev_b32_e32 v218, 16, v219
	v_and_b32_e32 v219, 0xffff0000, v219
	v_max_f32_e32 v212, 0x1e3ce508, v212
	v_max_f32_e32 v213, 0x1e3ce508, v213
	v_max_f32_e32 v214, 0x1e3ce508, v214
	v_max_f32_e32 v215, 0x1e3ce508, v215
	v_max_f32_e32 v216, 0x1e3ce508, v216
	v_max_f32_e32 v217, 0x1e3ce508, v217
	v_max_f32_e32 v218, 0x1e3ce508, v218
	v_max_f32_e32 v219, 0x1e3ce508, v219
	v_rcp_f32_e32 v212, v212
	v_rcp_f32_e32 v213, v213
	v_rcp_f32_e32 v214, v214
	v_rcp_f32_e32 v215, v215
	v_rcp_f32_e32 v216, v216
	v_rcp_f32_e32 v217, v217
	v_rcp_f32_e32 v218, v218
	v_rcp_f32_e32 v219, v219
	v_pk_mul_f32 v[168:169], v[168:169], v[212:213]
	v_pk_mul_f32 v[170:171], v[170:171], v[214:215]
	v_pk_mul_f32 v[224:225], v[224:225], v[216:217]
	v_pk_mul_f32 v[226:227], v[226:227], v[218:219]
	v_pk_mul_f32 v[88:89], v[88:89], v[168:169]
	v_pk_mul_f32 v[90:91], v[90:91], v[170:171]
	v_pk_mul_f32 v[84:85], v[84:85], v[224:225]
	v_pk_mul_f32 v[86:87], v[86:87], v[226:227]
	s_add_u32 s28, s26, 0xf0000
	s_addc_u32 s29, s27, 0
	global_load_dwordx4 v[196:199], v191, s[28:29] offset:256
	global_load_dwordx4 v[212:215], v191, s[28:29] offset:2304
	s_waitcnt vmcnt(12)
	v_lshlrev_b32_e32 v168, 16, v220
	v_and_b32_e32 v169, 0xffff0000, v220
	v_lshlrev_b32_e32 v170, 16, v221
	v_and_b32_e32 v171, 0xffff0000, v221
	v_lshlrev_b32_e32 v224, 16, v222
	v_and_b32_e32 v225, 0xffff0000, v222
	v_lshlrev_b32_e32 v226, 16, v223
	v_and_b32_e32 v227, 0xffff0000, v223
	v_max_f32_e32 v168, 0x1e3ce508, v168
	v_max_f32_e32 v169, 0x1e3ce508, v169
	v_max_f32_e32 v170, 0x1e3ce508, v170
	v_max_f32_e32 v171, 0x1e3ce508, v171
	v_max_f32_e32 v224, 0x1e3ce508, v224
	v_max_f32_e32 v225, 0x1e3ce508, v225
	v_max_f32_e32 v226, 0x1e3ce508, v226
	v_max_f32_e32 v227, 0x1e3ce508, v227
	v_lshlrev_b32_e32 v220, 16, v132
	v_and_b32_e32 v221, 0xffff0000, v132
	v_lshlrev_b32_e32 v222, 16, v133
	v_and_b32_e32 v223, 0xffff0000, v133
	v_lshlrev_b32_e32 v132, 16, v134
	v_and_b32_e32 v133, 0xffff0000, v134
	v_lshlrev_b32_e32 v134, 16, v135
	v_and_b32_e32 v135, 0xffff0000, v135
	v_max_f32_e32 v220, 0x1e3ce508, v220
	v_max_f32_e32 v221, 0x1e3ce508, v221
	v_max_f32_e32 v222, 0x1e3ce508, v222
	v_max_f32_e32 v223, 0x1e3ce508, v223
	v_max_f32_e32 v132, 0x1e3ce508, v132
	v_max_f32_e32 v133, 0x1e3ce508, v133
	v_max_f32_e32 v134, 0x1e3ce508, v134
	v_max_f32_e32 v135, 0x1e3ce508, v135
	v_rcp_f32_e32 v220, v220
	v_rcp_f32_e32 v221, v221
	v_rcp_f32_e32 v222, v222
	v_rcp_f32_e32 v223, v223
	v_rcp_f32_e32 v132, v132
	v_rcp_f32_e32 v133, v133
	v_rcp_f32_e32 v134, v134
	v_rcp_f32_e32 v135, v135
	v_pk_mul_f32 v[168:169], v[168:169], v[220:221]
	v_pk_mul_f32 v[170:171], v[170:171], v[222:223]
	v_pk_mul_f32 v[224:225], v[224:225], v[132:133]
	v_pk_mul_f32 v[226:227], v[226:227], v[134:135]
	v_pk_mul_f32 v[56:57], v[56:57], v[168:169]
	v_pk_mul_f32 v[58:59], v[58:59], v[170:171]
	v_pk_mul_f32 v[48:49], v[48:49], v[224:225]
	v_pk_mul_f32 v[50:51], v[50:51], v[226:227]
	s_add_u32 s28, s26, 0x108000
	s_addc_u32 s29, s27, 0
	global_load_dwordx4 v[216:219], v191, s[28:29]
	global_load_dwordx4 v[220:223], v191, s[28:29] offset:2048
	s_waitcnt vmcnt(12)
	v_lshlrev_b32_e32 v168, 16, v136
	v_and_b32_e32 v169, 0xffff0000, v136
	v_lshlrev_b32_e32 v170, 16, v137
	v_and_b32_e32 v171, 0xffff0000, v137
	v_lshlrev_b32_e32 v224, 16, v138
	v_and_b32_e32 v225, 0xffff0000, v138
	v_lshlrev_b32_e32 v226, 16, v139
	v_and_b32_e32 v227, 0xffff0000, v139
	v_max_f32_e32 v168, 0x1e3ce508, v168
	v_max_f32_e32 v169, 0x1e3ce508, v169
	v_max_f32_e32 v170, 0x1e3ce508, v170
	v_max_f32_e32 v171, 0x1e3ce508, v171
	v_max_f32_e32 v224, 0x1e3ce508, v224
	v_max_f32_e32 v225, 0x1e3ce508, v225
	v_max_f32_e32 v226, 0x1e3ce508, v226
	v_max_f32_e32 v227, 0x1e3ce508, v227
	v_lshlrev_b32_e32 v136, 16, v140
	v_and_b32_e32 v137, 0xffff0000, v140
	v_lshlrev_b32_e32 v138, 16, v141
	v_and_b32_e32 v139, 0xffff0000, v141
	v_lshlrev_b32_e32 v140, 16, v142
	v_and_b32_e32 v141, 0xffff0000, v142
	v_lshlrev_b32_e32 v142, 16, v143
	v_and_b32_e32 v143, 0xffff0000, v143
	v_max_f32_e32 v136, 0x1e3ce508, v136
	v_max_f32_e32 v137, 0x1e3ce508, v137
	v_max_f32_e32 v138, 0x1e3ce508, v138
	v_max_f32_e32 v139, 0x1e3ce508, v139
	v_max_f32_e32 v140, 0x1e3ce508, v140
	v_max_f32_e32 v141, 0x1e3ce508, v141
	v_max_f32_e32 v142, 0x1e3ce508, v142
	v_max_f32_e32 v143, 0x1e3ce508, v143
	v_rcp_f32_e32 v136, v136
	v_rcp_f32_e32 v137, v137
	v_rcp_f32_e32 v138, v138
	v_rcp_f32_e32 v139, v139
	v_rcp_f32_e32 v140, v140
	v_rcp_f32_e32 v141, v141
	v_rcp_f32_e32 v142, v142
	v_rcp_f32_e32 v143, v143
	v_pk_mul_f32 v[168:169], v[168:169], v[136:137]
	v_pk_mul_f32 v[170:171], v[170:171], v[138:139]
	v_pk_mul_f32 v[224:225], v[224:225], v[140:141]
	v_pk_mul_f32 v[226:227], v[226:227], v[142:143]
	v_pk_mul_f32 v[52:53], v[52:53], v[168:169]
	v_pk_mul_f32 v[54:55], v[54:55], v[170:171]
	v_pk_mul_f32 v[44:45], v[44:45], v[224:225]
	v_pk_mul_f32 v[46:47], v[46:47], v[226:227]
	s_add_u32 s28, s26, 0x108000
	s_addc_u32 s29, s27, 0
	global_load_dwordx4 v[132:135], v191, s[28:29] offset:256
	global_load_dwordx4 v[136:139], v191, s[28:29] offset:2304
	s_waitcnt vmcnt(12)
	v_lshlrev_b32_e32 v168, 16, v144
	v_and_b32_e32 v169, 0xffff0000, v144
	v_lshlrev_b32_e32 v170, 16, v145
	v_and_b32_e32 v171, 0xffff0000, v145
	v_lshlrev_b32_e32 v224, 16, v146
	v_and_b32_e32 v225, 0xffff0000, v146
	v_lshlrev_b32_e32 v226, 16, v147
	v_and_b32_e32 v227, 0xffff0000, v147
	v_max_f32_e32 v168, 0x1e3ce508, v168
	v_max_f32_e32 v169, 0x1e3ce508, v169
	v_max_f32_e32 v170, 0x1e3ce508, v170
	v_max_f32_e32 v171, 0x1e3ce508, v171
	v_max_f32_e32 v224, 0x1e3ce508, v224
	v_max_f32_e32 v225, 0x1e3ce508, v225
	v_max_f32_e32 v226, 0x1e3ce508, v226
	v_max_f32_e32 v227, 0x1e3ce508, v227
	v_lshlrev_b32_e32 v144, 16, v148
	v_and_b32_e32 v145, 0xffff0000, v148
	v_lshlrev_b32_e32 v146, 16, v149
	v_and_b32_e32 v147, 0xffff0000, v149
	v_lshlrev_b32_e32 v148, 16, v150
	v_and_b32_e32 v149, 0xffff0000, v150
	v_lshlrev_b32_e32 v150, 16, v151
	v_and_b32_e32 v151, 0xffff0000, v151
	v_max_f32_e32 v144, 0x1e3ce508, v144
	v_max_f32_e32 v145, 0x1e3ce508, v145
	v_max_f32_e32 v146, 0x1e3ce508, v146
	v_max_f32_e32 v147, 0x1e3ce508, v147
	v_max_f32_e32 v148, 0x1e3ce508, v148
	v_max_f32_e32 v149, 0x1e3ce508, v149
	v_max_f32_e32 v150, 0x1e3ce508, v150
	v_max_f32_e32 v151, 0x1e3ce508, v151
	v_rcp_f32_e32 v144, v144
	v_rcp_f32_e32 v145, v145
	v_rcp_f32_e32 v146, v146
	v_rcp_f32_e32 v147, v147
	v_rcp_f32_e32 v148, v148
	v_rcp_f32_e32 v149, v149
	v_rcp_f32_e32 v150, v150
	v_rcp_f32_e32 v151, v151
	v_pk_mul_f32 v[168:169], v[168:169], v[144:145]
	v_pk_mul_f32 v[170:171], v[170:171], v[146:147]
	v_pk_mul_f32 v[224:225], v[224:225], v[148:149]
	v_pk_mul_f32 v[226:227], v[226:227], v[150:151]
	v_pk_mul_f32 v[16:17], v[16:17], v[168:169]
	v_pk_mul_f32 v[18:19], v[18:19], v[170:171]
	v_pk_mul_f32 v[12:13], v[12:13], v[224:225]
	v_pk_mul_f32 v[14:15], v[14:15], v[226:227]
	s_waitcnt vmcnt(10)
	v_lshlrev_b32_e32 v168, 16, v152
	v_and_b32_e32 v169, 0xffff0000, v152
	v_lshlrev_b32_e32 v170, 16, v153
	v_and_b32_e32 v171, 0xffff0000, v153
	v_lshlrev_b32_e32 v224, 16, v154
	v_and_b32_e32 v225, 0xffff0000, v154
	v_lshlrev_b32_e32 v226, 16, v155
	v_and_b32_e32 v227, 0xffff0000, v155
	v_max_f32_e32 v168, 0x1e3ce508, v168
	v_max_f32_e32 v169, 0x1e3ce508, v169
	v_max_f32_e32 v170, 0x1e3ce508, v170
	v_max_f32_e32 v171, 0x1e3ce508, v171
	v_max_f32_e32 v224, 0x1e3ce508, v224
	v_max_f32_e32 v225, 0x1e3ce508, v225
	v_max_f32_e32 v226, 0x1e3ce508, v226
	v_max_f32_e32 v227, 0x1e3ce508, v227
	v_lshlrev_b32_e32 v152, 16, v156
	v_and_b32_e32 v153, 0xffff0000, v156
	v_lshlrev_b32_e32 v154, 16, v157
	v_and_b32_e32 v155, 0xffff0000, v157
	v_lshlrev_b32_e32 v156, 16, v158
	v_and_b32_e32 v157, 0xffff0000, v158
	v_lshlrev_b32_e32 v158, 16, v159
	v_and_b32_e32 v159, 0xffff0000, v159
	v_max_f32_e32 v152, 0x1e3ce508, v152
	v_max_f32_e32 v153, 0x1e3ce508, v153
	v_max_f32_e32 v154, 0x1e3ce508, v154
	v_max_f32_e32 v155, 0x1e3ce508, v155
	v_max_f32_e32 v156, 0x1e3ce508, v156
	v_max_f32_e32 v157, 0x1e3ce508, v157
	v_max_f32_e32 v158, 0x1e3ce508, v158
	v_max_f32_e32 v159, 0x1e3ce508, v159
	v_rcp_f32_e32 v152, v152
	v_rcp_f32_e32 v153, v153
	v_rcp_f32_e32 v154, v154
	v_rcp_f32_e32 v155, v155
	v_rcp_f32_e32 v156, v156
	v_rcp_f32_e32 v157, v157
	v_rcp_f32_e32 v158, v158
	v_rcp_f32_e32 v159, v159
	v_pk_mul_f32 v[168:169], v[168:169], v[152:153]
	v_pk_mul_f32 v[170:171], v[170:171], v[154:155]
	v_pk_mul_f32 v[224:225], v[224:225], v[156:157]
	v_pk_mul_f32 v[226:227], v[226:227], v[158:159]
	v_pk_mul_f32 v[40:41], v[40:41], v[168:169]
	v_pk_mul_f32 v[42:43], v[42:43], v[170:171]
	v_pk_mul_f32 v[36:37], v[36:37], v[224:225]
	v_pk_mul_f32 v[38:39], v[38:39], v[226:227]
	s_waitcnt vmcnt(8)
	v_lshlrev_b32_e32 v168, 16, v160
	v_and_b32_e32 v169, 0xffff0000, v160
	v_lshlrev_b32_e32 v170, 16, v161
	v_and_b32_e32 v171, 0xffff0000, v161
	v_lshlrev_b32_e32 v224, 16, v162
	v_and_b32_e32 v225, 0xffff0000, v162
	v_lshlrev_b32_e32 v226, 16, v163
	v_and_b32_e32 v227, 0xffff0000, v163
	v_max_f32_e32 v168, 0x1e3ce508, v168
	v_max_f32_e32 v169, 0x1e3ce508, v169
	v_max_f32_e32 v170, 0x1e3ce508, v170
	v_max_f32_e32 v171, 0x1e3ce508, v171
	v_max_f32_e32 v224, 0x1e3ce508, v224
	v_max_f32_e32 v225, 0x1e3ce508, v225
	v_max_f32_e32 v226, 0x1e3ce508, v226
	v_max_f32_e32 v227, 0x1e3ce508, v227
	v_lshlrev_b32_e32 v160, 16, v180
	v_and_b32_e32 v161, 0xffff0000, v180
	v_lshlrev_b32_e32 v162, 16, v181
	v_and_b32_e32 v163, 0xffff0000, v181
	v_lshlrev_b32_e32 v180, 16, v182
	v_and_b32_e32 v181, 0xffff0000, v182
	v_lshlrev_b32_e32 v182, 16, v183
	v_and_b32_e32 v183, 0xffff0000, v183
	v_max_f32_e32 v160, 0x1e3ce508, v160
	v_max_f32_e32 v161, 0x1e3ce508, v161
	v_max_f32_e32 v162, 0x1e3ce508, v162
	v_max_f32_e32 v163, 0x1e3ce508, v163
	v_max_f32_e32 v180, 0x1e3ce508, v180
	v_max_f32_e32 v181, 0x1e3ce508, v181
	v_max_f32_e32 v182, 0x1e3ce508, v182
	v_max_f32_e32 v183, 0x1e3ce508, v183
	v_rcp_f32_e32 v160, v160
	v_rcp_f32_e32 v161, v161
	v_rcp_f32_e32 v162, v162
	v_rcp_f32_e32 v163, v163
	v_rcp_f32_e32 v180, v180
	v_rcp_f32_e32 v181, v181
	v_rcp_f32_e32 v182, v182
	v_rcp_f32_e32 v183, v183
	v_pk_mul_f32 v[168:169], v[168:169], v[160:161]
	v_pk_mul_f32 v[170:171], v[170:171], v[162:163]
	v_pk_mul_f32 v[224:225], v[224:225], v[180:181]
	v_pk_mul_f32 v[226:227], v[226:227], v[182:183]
	v_pk_mul_f32 v[8:9], v[8:9], v[168:169]
	v_pk_mul_f32 v[10:11], v[10:11], v[170:171]
	v_pk_mul_f32 v[4:5], v[4:5], v[224:225]
	v_pk_mul_f32 v[6:7], v[6:7], v[226:227]
	s_waitcnt vmcnt(6)
	v_lshlrev_b32_e32 v168, 16, v184
	v_and_b32_e32 v169, 0xffff0000, v184
	v_lshlrev_b32_e32 v170, 16, v185
	v_and_b32_e32 v171, 0xffff0000, v185
	v_lshlrev_b32_e32 v224, 16, v186
	v_and_b32_e32 v225, 0xffff0000, v186
	v_lshlrev_b32_e32 v226, 16, v187
	v_and_b32_e32 v227, 0xffff0000, v187
	v_max_f32_e32 v168, 0x1e3ce508, v168
	v_max_f32_e32 v169, 0x1e3ce508, v169
	v_max_f32_e32 v170, 0x1e3ce508, v170
	v_max_f32_e32 v171, 0x1e3ce508, v171
	v_max_f32_e32 v224, 0x1e3ce508, v224
	v_max_f32_e32 v225, 0x1e3ce508, v225
	v_max_f32_e32 v226, 0x1e3ce508, v226
	v_max_f32_e32 v227, 0x1e3ce508, v227
	v_lshlrev_b32_e32 v184, 16, v192
	v_and_b32_e32 v185, 0xffff0000, v192
	v_lshlrev_b32_e32 v186, 16, v193
	v_and_b32_e32 v187, 0xffff0000, v193
	v_lshlrev_b32_e32 v192, 16, v194
	v_and_b32_e32 v193, 0xffff0000, v194
	v_lshlrev_b32_e32 v194, 16, v195
	v_and_b32_e32 v195, 0xffff0000, v195
	v_max_f32_e32 v184, 0x1e3ce508, v184
	v_max_f32_e32 v185, 0x1e3ce508, v185
	v_max_f32_e32 v186, 0x1e3ce508, v186
	v_max_f32_e32 v187, 0x1e3ce508, v187
	v_max_f32_e32 v192, 0x1e3ce508, v192
	v_max_f32_e32 v193, 0x1e3ce508, v193
	v_max_f32_e32 v194, 0x1e3ce508, v194
	v_max_f32_e32 v195, 0x1e3ce508, v195
	v_rcp_f32_e32 v184, v184
	v_rcp_f32_e32 v185, v185
	v_rcp_f32_e32 v186, v186
	v_rcp_f32_e32 v187, v187
	v_rcp_f32_e32 v192, v192
	v_rcp_f32_e32 v193, v193
	v_rcp_f32_e32 v194, v194
	v_rcp_f32_e32 v195, v195
	v_pk_mul_f32 v[168:169], v[168:169], v[184:185]
	v_pk_mul_f32 v[170:171], v[170:171], v[186:187]
	v_pk_mul_f32 v[224:225], v[224:225], v[192:193]
	v_pk_mul_f32 v[226:227], v[226:227], v[194:195]
	v_pk_mul_f32 v[32:33], v[32:33], v[168:169]
	v_pk_mul_f32 v[34:35], v[34:35], v[170:171]
	v_pk_mul_f32 v[28:29], v[28:29], v[224:225]
	v_pk_mul_f32 v[30:31], v[30:31], v[226:227]
	s_waitcnt vmcnt(4)
	v_lshlrev_b32_e32 v168, 16, v196
	v_and_b32_e32 v169, 0xffff0000, v196
	v_lshlrev_b32_e32 v170, 16, v197
	v_and_b32_e32 v171, 0xffff0000, v197
	v_lshlrev_b32_e32 v224, 16, v198
	v_and_b32_e32 v225, 0xffff0000, v198
	v_lshlrev_b32_e32 v226, 16, v199
	v_and_b32_e32 v227, 0xffff0000, v199
	v_max_f32_e32 v168, 0x1e3ce508, v168
	v_max_f32_e32 v169, 0x1e3ce508, v169
	v_max_f32_e32 v170, 0x1e3ce508, v170
	v_max_f32_e32 v171, 0x1e3ce508, v171
	v_max_f32_e32 v224, 0x1e3ce508, v224
	v_max_f32_e32 v225, 0x1e3ce508, v225
	v_max_f32_e32 v226, 0x1e3ce508, v226
	v_max_f32_e32 v227, 0x1e3ce508, v227
	v_lshlrev_b32_e32 v196, 16, v212
	v_and_b32_e32 v197, 0xffff0000, v212
	v_lshlrev_b32_e32 v198, 16, v213
	v_and_b32_e32 v199, 0xffff0000, v213
	v_lshlrev_b32_e32 v212, 16, v214
	v_and_b32_e32 v213, 0xffff0000, v214
	v_lshlrev_b32_e32 v214, 16, v215
	v_and_b32_e32 v215, 0xffff0000, v215
	v_max_f32_e32 v196, 0x1e3ce508, v196
	v_max_f32_e32 v197, 0x1e3ce508, v197
	v_max_f32_e32 v198, 0x1e3ce508, v198
	v_max_f32_e32 v199, 0x1e3ce508, v199
	v_max_f32_e32 v212, 0x1e3ce508, v212
	v_max_f32_e32 v213, 0x1e3ce508, v213
	v_max_f32_e32 v214, 0x1e3ce508, v214
	v_max_f32_e32 v215, 0x1e3ce508, v215
	v_rcp_f32_e32 v196, v196
	v_rcp_f32_e32 v197, v197
	v_rcp_f32_e32 v198, v198
	v_rcp_f32_e32 v199, v199
	v_rcp_f32_e32 v212, v212
	v_rcp_f32_e32 v213, v213
	v_rcp_f32_e32 v214, v214
	v_rcp_f32_e32 v215, v215
	v_pk_mul_f32 v[168:169], v[168:169], v[196:197]
	v_pk_mul_f32 v[170:171], v[170:171], v[198:199]
	v_pk_mul_f32 v[224:225], v[224:225], v[212:213]
	v_pk_mul_f32 v[226:227], v[226:227], v[214:215]
	v_pk_mul_f32 v[116:117], v[116:117], v[168:169]
	v_pk_mul_f32 v[118:119], v[118:119], v[170:171]
	v_pk_mul_f32 v[120:121], v[120:121], v[224:225]
	v_pk_mul_f32 v[122:123], v[122:123], v[226:227]
	s_waitcnt vmcnt(2)
	v_lshlrev_b32_e32 v168, 16, v216
	v_and_b32_e32 v169, 0xffff0000, v216
	v_lshlrev_b32_e32 v170, 16, v217
	v_and_b32_e32 v171, 0xffff0000, v217
	v_lshlrev_b32_e32 v224, 16, v218
	v_and_b32_e32 v225, 0xffff0000, v218
	v_lshlrev_b32_e32 v226, 16, v219
	v_and_b32_e32 v227, 0xffff0000, v219
	v_max_f32_e32 v168, 0x1e3ce508, v168
	v_max_f32_e32 v169, 0x1e3ce508, v169
	v_max_f32_e32 v170, 0x1e3ce508, v170
	v_max_f32_e32 v171, 0x1e3ce508, v171
	v_max_f32_e32 v224, 0x1e3ce508, v224
	v_max_f32_e32 v225, 0x1e3ce508, v225
	v_max_f32_e32 v226, 0x1e3ce508, v226
	v_max_f32_e32 v227, 0x1e3ce508, v227
	v_lshlrev_b32_e32 v216, 16, v220
	v_and_b32_e32 v217, 0xffff0000, v220
	v_lshlrev_b32_e32 v218, 16, v221
	v_and_b32_e32 v219, 0xffff0000, v221
	v_lshlrev_b32_e32 v220, 16, v222
	v_and_b32_e32 v221, 0xffff0000, v222
	v_lshlrev_b32_e32 v222, 16, v223
	v_and_b32_e32 v223, 0xffff0000, v223
	v_max_f32_e32 v216, 0x1e3ce508, v216
	v_max_f32_e32 v217, 0x1e3ce508, v217
	v_max_f32_e32 v218, 0x1e3ce508, v218
	v_max_f32_e32 v219, 0x1e3ce508, v219
	v_max_f32_e32 v220, 0x1e3ce508, v220
	v_max_f32_e32 v221, 0x1e3ce508, v221
	v_max_f32_e32 v222, 0x1e3ce508, v222
	v_max_f32_e32 v223, 0x1e3ce508, v223
	v_rcp_f32_e32 v216, v216
	v_rcp_f32_e32 v217, v217
	v_rcp_f32_e32 v218, v218
	v_rcp_f32_e32 v219, v219
	v_rcp_f32_e32 v220, v220
	v_rcp_f32_e32 v221, v221
	v_rcp_f32_e32 v222, v222
	v_rcp_f32_e32 v223, v223
	v_pk_mul_f32 v[168:169], v[168:169], v[216:217]
	v_pk_mul_f32 v[170:171], v[170:171], v[218:219]
	v_pk_mul_f32 v[224:225], v[224:225], v[220:221]
	v_pk_mul_f32 v[226:227], v[226:227], v[222:223]
	v_pk_mul_f32 v[24:25], v[24:25], v[168:169]
	v_pk_mul_f32 v[26:27], v[26:27], v[170:171]
	v_pk_mul_f32 v[20:21], v[20:21], v[224:225]
	v_pk_mul_f32 v[22:23], v[22:23], v[226:227]
	s_waitcnt vmcnt(0)
	v_lshlrev_b32_e32 v168, 16, v132
	v_and_b32_e32 v169, 0xffff0000, v132
	v_lshlrev_b32_e32 v170, 16, v133
	v_and_b32_e32 v171, 0xffff0000, v133
	v_lshlrev_b32_e32 v224, 16, v134
	v_and_b32_e32 v225, 0xffff0000, v134
	v_lshlrev_b32_e32 v226, 16, v135
	v_and_b32_e32 v227, 0xffff0000, v135
	v_max_f32_e32 v168, 0x1e3ce508, v168
	v_max_f32_e32 v169, 0x1e3ce508, v169
	v_max_f32_e32 v170, 0x1e3ce508, v170
	v_max_f32_e32 v171, 0x1e3ce508, v171
	v_max_f32_e32 v224, 0x1e3ce508, v224
	v_max_f32_e32 v225, 0x1e3ce508, v225
	v_max_f32_e32 v226, 0x1e3ce508, v226
	v_max_f32_e32 v227, 0x1e3ce508, v227
	v_lshlrev_b32_e32 v132, 16, v136
	v_and_b32_e32 v133, 0xffff0000, v136
	v_lshlrev_b32_e32 v134, 16, v137
	v_and_b32_e32 v135, 0xffff0000, v137
	v_lshlrev_b32_e32 v136, 16, v138
	v_and_b32_e32 v137, 0xffff0000, v138
	v_lshlrev_b32_e32 v138, 16, v139
	v_and_b32_e32 v139, 0xffff0000, v139
	v_max_f32_e32 v132, 0x1e3ce508, v132
	v_max_f32_e32 v133, 0x1e3ce508, v133
	v_max_f32_e32 v134, 0x1e3ce508, v134
	v_max_f32_e32 v135, 0x1e3ce508, v135
	v_max_f32_e32 v136, 0x1e3ce508, v136
	v_max_f32_e32 v137, 0x1e3ce508, v137
	v_max_f32_e32 v138, 0x1e3ce508, v138
	v_max_f32_e32 v139, 0x1e3ce508, v139
	v_rcp_f32_e32 v132, v132
	v_rcp_f32_e32 v133, v133
	v_rcp_f32_e32 v134, v134
	v_rcp_f32_e32 v135, v135
	v_rcp_f32_e32 v136, v136
	v_rcp_f32_e32 v137, v137
	v_rcp_f32_e32 v138, v138
	v_rcp_f32_e32 v139, v139
	v_pk_mul_f32 v[168:169], v[168:169], v[132:133]
	v_pk_mul_f32 v[170:171], v[170:171], v[134:135]
	v_pk_mul_f32 v[224:225], v[224:225], v[136:137]
	v_pk_mul_f32 v[226:227], v[226:227], v[138:139]
	v_pk_mul_f32 v[124:125], v[124:125], v[168:169]
	v_pk_mul_f32 v[126:127], v[126:127], v[170:171]
	v_pk_mul_f32 v[128:129], v[128:129], v[224:225]
	v_pk_mul_f32 v[130:131], v[130:131], v[226:227]
	s_branch .Lmg_done
.Lmg_mid:
	s_add_u32 s28, s26, 0x0
	s_addc_u32 s29, s27, 0
	global_load_dwordx4 v[136:139], v191, s[28:29] offset:2048
	s_add_u32 s28, s26, 0x0
	s_addc_u32 s29, s27, 0
	global_load_dwordx4 v[144:147], v191, s[28:29] offset:2304
	s_add_u32 s28, s26, 0x18000
	s_addc_u32 s29, s27, 0
	global_load_dwordx4 v[152:155], v191, s[28:29] offset:2048
	s_add_u32 s28, s26, 0x18000
	s_addc_u32 s29, s27, 0
	global_load_dwordx4 v[160:163], v191, s[28:29] offset:2304
	s_add_u32 s28, s26, 0x30000
	s_addc_u32 s29, s27, 0
	global_load_dwordx4 v[184:187], v191, s[28:29] offset:2048
	s_add_u32 s28, s26, 0x30000
	s_addc_u32 s29, s27, 0
	global_load_dwordx4 v[196:199], v191, s[28:29] offset:2304
	s_add_u32 s28, s26, 0x48000
	s_addc_u32 s29, s27, 0
	global_load_dwordx4 v[212:215], v191, s[28:29]
	global_load_dwordx4 v[216:219], v191, s[28:29] offset:2048
	s_and_b64 vcc, exec, s[20:21]
	s_cbranch_vccz .Lmg_nbm
	s_barrier
.Lmg_nbm:
	s_waitcnt vmcnt(7)
	v_lshlrev_b32_e32 v168, 16, v228
	v_and_b32_e32 v169, 0xffff0000, v228
	v_lshlrev_b32_e32 v170, 16, v229
	v_and_b32_e32 v171, 0xffff0000, v229
	v_lshlrev_b32_e32 v224, 16, v230
	v_and_b32_e32 v225, 0xffff0000, v230
	v_lshlrev_b32_e32 v226, 16, v231
	v_and_b32_e32 v227, 0xffff0000, v231
	v_max_f32_e32 v168, 0x1e3ce508, v168
	v_max_f32_e32 v169, 0x1e3ce508, v169
	v_max_f32_e32 v170, 0x1e3ce508, v170
	v_max_f32_e32 v171, 0x1e3ce508, v171
	v_max_f32_e32 v224, 0x1e3ce508, v224
	v_max_f32_e32 v225, 0x1e3ce508, v225
	v_max_f32_e32 v226, 0x1e3ce508, v226
	v_max_f32_e32 v227, 0x1e3ce508, v227
	v_mov_b32_e32 v228, v136
	v_mov_b32_e32 v229, v137
	v_mov_b32_e32 v230, v138
	v_mov_b32_e32 v231, v139
	v_lshlrev_b32_e32 v132, 16, v136
	v_and_b32_e32 v133, 0xffff0000, v136
	v_lshlrev_b32_e32 v134, 16, v137
	v_and_b32_e32 v135, 0xffff0000, v137
	v_lshlrev_b32_e32 v136, 16, v138
	v_and_b32_e32 v137, 0xffff0000, v138
	v_lshlrev_b32_e32 v138, 16, v139
	v_and_b32_e32 v139, 0xffff0000, v139
	v_max_f32_e32 v132, 0x1e3ce508, v132
	v_max_f32_e32 v133, 0x1e3ce508, v133
	v_max_f32_e32 v134, 0x1e3ce508, v134
	v_max_f32_e32 v135, 0x1e3ce508, v135
	v_max_f32_e32 v136, 0x1e3ce508, v136
	v_max_f32_e32 v137, 0x1e3ce508, v137
	v_max_f32_e32 v138, 0x1e3ce508, v138
	v_max_f32_e32 v139, 0x1e3ce508, v139
	v_rcp_f32_e32 v132, v132
	v_rcp_f32_e32 v133, v133
	v_rcp_f32_e32 v134, v134
	v_rcp_f32_e32 v135, v135
	v_rcp_f32_e32 v136, v136
	v_rcp_f32_e32 v137, v137
	v_rcp_f32_e32 v138, v138
	v_rcp_f32_e32 v139, v139
	v_pk_mul_f32 v[168:169], v[168:169], v[132:133]
	v_pk_mul_f32 v[170:171], v[170:171], v[134:135]
	v_pk_mul_f32 v[224:225], v[224:225], v[136:137]
	v_pk_mul_f32 v[226:227], v[226:227], v[138:139]
	v_pk_mul_f32 v[112:113], v[112:113], v[168:169]
	v_pk_mul_f32 v[114:115], v[114:115], v[170:171]
	v_pk_mul_f32 v[108:109], v[108:109], v[224:225]
	v_pk_mul_f32 v[110:111], v[110:111], v[226:227]
	s_add_u32 s28, s26, 0x48000
	s_addc_u32 s29, s27, 0
	global_load_dwordx4 v[220:223], v191, s[28:29] offset:256
	global_load_dwordx4 v[132:135], v191, s[28:29] offset:2304
	s_waitcnt vmcnt(8)
	v_lshlrev_b32_e32 v168, 16, v232
	v_and_b32_e32 v169, 0xffff0000, v232
	v_lshlrev_b32_e32 v170, 16, v233
	v_and_b32_e32 v171, 0xffff0000, v233
	v_lshlrev_b32_e32 v224, 16, v234
	v_and_b32_e32 v225, 0xffff0000, v234
	v_lshlrev_b32_e32 v226, 16, v235
	v_and_b32_e32 v227, 0xffff0000, v235
	v_max_f32_e32 v168, 0x1e3ce508, v168
	v_max_f32_e32 v169, 0x1e3ce508, v169
	v_max_f32_e32 v170, 0x1e3ce508, v170
	v_max_f32_e32 v171, 0x1e3ce508, v171
	v_max_f32_e32 v224, 0x1e3ce508, v224
	v_max_f32_e32 v225, 0x1e3ce508, v225
	v_max_f32_e32 v226, 0x1e3ce508, v226
	v_max_f32_e32 v227, 0x1e3ce508, v227
	v_mov_b32_e32 v232, v144
	v_mov_b32_e32 v233, v145
	v_mov_b32_e32 v234, v146
	v_mov_b32_e32 v235, v147
	v_lshlrev_b32_e32 v140, 16, v144
	v_and_b32_e32 v141, 0xffff0000, v144
	v_lshlrev_b32_e32 v142, 16, v145
	v_and_b32_e32 v143, 0xffff0000, v145
	v_lshlrev_b32_e32 v144, 16, v146
	v_and_b32_e32 v145, 0xffff0000, v146
	v_lshlrev_b32_e32 v146, 16, v147
	v_and_b32_e32 v147, 0xffff0000, v147
	v_max_f32_e32 v140, 0x1e3ce508, v140
	v_max_f32_e32 v141, 0x1e3ce508, v141
	v_max_f32_e32 v142, 0x1e3ce508, v142
	v_max_f32_e32 v143, 0x1e3ce508, v143
	v_max_f32_e32 v144, 0x1e3ce508, v144
	v_max_f32_e32 v145, 0x1e3ce508, v145
	v_max_f32_e32 v146, 0x1e3ce508, v146
	v_max_f32_e32 v147, 0x1e3ce508, v147
	v_rcp_f32_e32 v140, v140
	v_rcp_f32_e32 v141, v141
	v_rcp_f32_e32 v142, v142
	v_rcp_f32_e32 v143, v143
	v_rcp_f32_e32 v144, v144
	v_rcp_f32_e32 v145, v145
	v_rcp_f32_e32 v146, v146
	v_rcp_f32_e32 v147, v147
	v_pk_mul_f32 v[168:169], v[168:169], v[140:141]
	v_pk_mul_f32 v[170:171], v[170:171], v[142:143]
	v_pk_mul_f32 v[224:225], v[224:225], v[144:145]
	v_pk_mul_f32 v[226:227], v[226:227], v[146:147]
	v_pk_mul_f32 v[80:81], v[80:81], v[168:169]
	v_pk_mul_f32 v[82:83], v[82:83], v[170:171]
	v_pk_mul_f32 v[76:77], v[76:77], v[224:225]
	v_pk_mul_f32 v[78:79], v[78:79], v[226:227]
	s_add_u32 s28, s26, 0xc0000
	s_addc_u32 s29, s27, 0
	global_load_dwordx4 v[136:139], v191, s[28:29]
	global_load_dwordx4 v[140:143], v191, s[28:29] offset:2048
	s_waitcnt vmcnt(9)
	v_lshlrev_b32_e32 v168, 16, v236
	v_and_b32_e32 v169, 0xffff0000, v236
	v_lshlrev_b32_e32 v170, 16, v237
	v_and_b32_e32 v171, 0xffff0000, v237
	v_lshlrev_b32_e32 v224, 16, v238
	v_and_b32_e32 v225, 0xffff0000, v238
	v_lshlrev_b32_e32 v226, 16, v239
	v_and_b32_e32 v227, 0xffff0000, v239
	v_max_f32_e32 v168, 0x1e3ce508, v168
	v_max_f32_e32 v169, 0x1e3ce508, v169
	v_max_f32_e32 v170, 0x1e3ce508, v170
	v_max_f32_e32 v171, 0x1e3ce508, v171
	v_max_f32_e32 v224, 0x1e3ce508, v224
	v_max_f32_e32 v225, 0x1e3ce508, v225
	v_max_f32_e32 v226, 0x1e3ce508, v226
	v_max_f32_e32 v227, 0x1e3ce508, v227
	v_mov_b32_e32 v236, v152
	v_mov_b32_e32 v237, v153
	v_mov_b32_e32 v238, v154
	v_mov_b32_e32 v239, v155
	v_lshlrev_b32_e32 v148, 16, v152
	v_and_b32_e32 v149, 0xffff0000, v152
	v_lshlrev_b32_e32 v150, 16, v153
	v_and_b32_e32 v151, 0xffff0000, v153
	v_lshlrev_b32_e32 v152, 16, v154
	v_and_b32_e32 v153, 0xffff0000, v154
	v_lshlrev_b32_e32 v154, 16, v155
	v_and_b32_e32 v155, 0xffff0000, v155
	v_max_f32_e32 v148, 0x1e3ce508, v148
	v_max_f32_e32 v149, 0x1e3ce508, v149
	v_max_f32_e32 v150, 0x1e3ce508, v150
	v_max_f32_e32 v151, 0x1e3ce508, v151
	v_max_f32_e32 v152, 0x1e3ce508, v152
	v_max_f32_e32 v153, 0x1e3ce508, v153
	v_max_f32_e32 v154, 0x1e3ce508, v154
	v_max_f32_e32 v155, 0x1e3ce508, v155
	v_rcp_f32_e32 v148, v148
	v_rcp_f32_e32 v149, v149
	v_rcp_f32_e32 v150, v150
	v_rcp_f32_e32 v151, v151
	v_rcp_f32_e32 v152, v152
	v_rcp_f32_e32 v153, v153
	v_rcp_f32_e32 v154, v154
	v_rcp_f32_e32 v155, v155
	v_pk_mul_f32 v[168:169], v[168:169], v[148:149]
	v_pk_mul_f32 v[170:171], v[170:171], v[150:151]
	v_pk_mul_f32 v[224:225], v[224:225], v[152:153]
	v_pk_mul_f32 v[226:227], v[226:227], v[154:155]
	v_pk_mul_f32 v[104:105], v[104:105], v[168:169]
	v_pk_mul_f32 v[106:107], v[106:107], v[170:171]
	v_pk_mul_f32 v[100:101], v[100:101], v[224:225]
	v_pk_mul_f32 v[102:103], v[102:103], v[226:227]
	s_add_u32 s28, s26, 0xc0000
	s_addc_u32 s29, s27, 0
	global_load_dwordx4 v[144:147], v191, s[28:29] offset:256
	global_load_dwordx4 v[148:151], v191, s[28:29] offset:2304
	s_waitcnt vmcnt(10)
	v_lshlrev_b32_e32 v168, 16, v240
	v_and_b32_e32 v169, 0xffff0000, v240
	v_lshlrev_b32_e32 v170, 16, v241
	v_and_b32_e32 v171, 0xffff0000, v241
	v_lshlrev_b32_e32 v224, 16, v242
	v_and_b32_e32 v225, 0xffff0000, v242
	v_lshlrev_b32_e32 v226, 16, v243
	v_and_b32_e32 v227, 0xffff0000, v243
	v_max_f32_e32 v168, 0x1e3ce508, v168
	v_max_f32_e32 v169, 0x1e3ce508, v169
	v_max_f32_e32 v170, 0x1e3ce508, v170
	v_max_f32_e32 v171, 0x1e3ce508, v171
	v_max_f32_e32 v224, 0x1e3ce508, v224
	v_max_f32_e32 v225, 0x1e3ce508, v225
	v_max_f32_e32 v226, 0x1e3ce508, v226
	v_max_f32_e32 v227, 0x1e3ce508, v227
	v_mov_b32_e32 v240, v160
	v_mov_b32_e32 v241, v161
	v_mov_b32_e32 v242, v162
	v_mov_b32_e32 v243, v163
	v_lshlrev_b32_e32 v156, 16, v160
	v_and_b32_e32 v157, 0xffff0000, v160
	v_lshlrev_b32_e32 v158, 16, v161
	v_and_b32_e32 v159, 0xffff0000, v161
	v_lshlrev_b32_e32 v160, 16, v162
	v_and_b32_e32 v161, 0xffff0000, v162
	v_lshlrev_b32_e32 v162, 16, v163
	v_and_b32_e32 v163, 0xffff0000, v163
	v_max_f32_e32 v156, 0x1e3ce508, v156
	v_max_f32_e32 v157, 0x1e3ce508, v157
	v_max_f32_e32 v158, 0x1e3ce508, v158
	v_max_f32_e32 v159, 0x1e3ce508, v159
	v_max_f32_e32 v160, 0x1e3ce508, v160
	v_max_f32_e32 v161, 0x1e3ce508, v161
	v_max_f32_e32 v162, 0x1e3ce508, v162
	v_max_f32_e32 v163, 0x1e3ce508, v163
	v_rcp_f32_e32 v156, v156
	v_rcp_f32_e32 v157, v157
	v_rcp_f32_e32 v158, v158
	v_rcp_f32_e32 v159, v159
	v_rcp_f32_e32 v160, v160
	v_rcp_f32_e32 v161, v161
	v_rcp_f32_e32 v162, v162
	v_rcp_f32_e32 v163, v163
	v_pk_mul_f32 v[168:169], v[168:169], v[156:157]
	v_pk_mul_f32 v[170:171], v[170:171], v[158:159]
	v_pk_mul_f32 v[224:225], v[224:225], v[160:161]
	v_pk_mul_f32 v[226:227], v[226:227], v[162:163]
	v_pk_mul_f32 v[72:73], v[72:73], v[168:169]
	v_pk_mul_f32 v[74:75], v[74:75], v[170:171]
	v_pk_mul_f32 v[68:69], v[68:69], v[224:225]
	v_pk_mul_f32 v[70:71], v[70:71], v[226:227]
	s_add_u32 s28, s26, 0xd8000
	s_addc_u32 s29, s27, 0
	global_load_dwordx4 v[152:155], v191, s[28:29]
	global_load_dwordx4 v[156:159], v191, s[28:29] offset:2048
	s_waitcnt vmcnt(11)
	v_lshlrev_b32_e32 v168, 16, v244
	v_and_b32_e32 v169, 0xffff0000, v244
	v_lshlrev_b32_e32 v170, 16, v245
	v_and_b32_e32 v171, 0xffff0000, v245
	v_lshlrev_b32_e32 v224, 16, v246
	v_and_b32_e32 v225, 0xffff0000, v246
	v_lshlrev_b32_e32 v226, 16, v247
	v_and_b32_e32 v227, 0xffff0000, v247
	v_max_f32_e32 v168, 0x1e3ce508, v168
	v_max_f32_e32 v169, 0x1e3ce508, v169
	v_max_f32_e32 v170, 0x1e3ce508, v170
	v_max_f32_e32 v171, 0x1e3ce508, v171
	v_max_f32_e32 v224, 0x1e3ce508, v224
	v_max_f32_e32 v225, 0x1e3ce508, v225
	v_max_f32_e32 v226, 0x1e3ce508, v226
	v_max_f32_e32 v227, 0x1e3ce508, v227
	v_mov_b32_e32 v244, v184
	v_mov_b32_e32 v245, v185
	v_mov_b32_e32 v246, v186
	v_mov_b32_e32 v247, v187
	v_lshlrev_b32_e32 v180, 16, v184
	v_and_b32_e32 v181, 0xffff0000, v184
	v_lshlrev_b32_e32 v182, 16, v185
	v_and_b32_e32 v183, 0xffff0000, v185
	v_lshlrev_b32_e32 v184, 16, v186
	v_and_b32_e32 v185, 0xffff0000, v186
	v_lshlrev_b32_e32 v186, 16, v187
	v_and_b32_e32 v187, 0xffff0000, v187
	v_max_f32_e32 v180, 0x1e3ce508, v180
	v_max_f32_e32 v181, 0x1e3ce508, v181
	v_max_f32_e32 v182, 0x1e3ce508, v182
	v_max_f32_e32 v183, 0x1e3ce508, v183
	v_max_f32_e32 v184, 0x1e3ce508, v184
	v_max_f32_e32 v185, 0x1e3ce508, v185
	v_max_f32_e32 v186, 0x1e3ce508, v186
	v_max_f32_e32 v187, 0x1e3ce508, v187
	v_rcp_f32_e32 v180, v180
	v_rcp_f32_e32 v181, v181
	v_rcp_f32_e32 v182, v182
	v_rcp_f32_e32 v183, v183
	v_rcp_f32_e32 v184, v184
	v_rcp_f32_e32 v185, v185
	v_rcp_f32_e32 v186, v186
	v_rcp_f32_e32 v187, v187
	v_pk_mul_f32 v[168:169], v[168:169], v[180:181]
	v_pk_mul_f32 v[170:171], v[170:171], v[182:183]
	v_pk_mul_f32 v[224:225], v[224:225], v[184:185]
	v_pk_mul_f32 v[226:227], v[226:227], v[186:187]
	v_pk_mul_f32 v[96:97], v[96:97], v[168:169]
	v_pk_mul_f32 v[98:99], v[98:99], v[170:171]
	v_pk_mul_f32 v[92:93], v[92:93], v[224:225]
	v_pk_mul_f32 v[94:95], v[94:95], v[226:227]
	s_add_u32 s28, s26, 0xd8000
	s_addc_u32 s29, s27, 0
	global_load_dwordx4 v[160:163], v191, s[28:29] offset:256
	global_load_dwordx4 v[180:183], v191, s[28:29] offset:2304
	s_waitcnt vmcnt(12)
	v_lshlrev_b32_e32 v168, 16, v248
	v_and_b32_e32 v169, 0xffff0000, v248
	v_lshlrev_b32_e32 v170, 16, v249
	v_and_b32_e32 v171, 0xffff0000, v249
	v_lshlrev_b32_e32 v224, 16, v250
	v_and_b32_e32 v225, 0xffff0000, v250
	v_lshlrev_b32_e32 v226, 16, v251
	v_and_b32_e32 v227, 0xffff0000, v251
	v_max_f32_e32 v168, 0x1e3ce508, v168
	v_max_f32_e32 v169, 0x1e3ce508, v169
	v_max_f32_e32 v170, 0x1e3ce508, v170
	v_max_f32_e32 v171, 0x1e3ce508, v171
	v_max_f32_e32 v224, 0x1e3ce508, v224
	v_max_f32_e32 v225, 0x1e3ce508, v225
	v_max_f32_e32 v226, 0x1e3ce508, v226
	v_max_f32_e32 v227, 0x1e3ce508, v227
	v_mov_b32_e32 v248, v196
	v_mov_b32_e32 v249, v197
	v_mov_b32_e32 v250, v198
	v_mov_b32_e32 v251, v199
	v_lshlrev_b32_e32 v192, 16, v196
	v_and_b32_e32 v193, 0xffff0000, v196
	v_lshlrev_b32_e32 v194, 16, v197
	v_and_b32_e32 v195, 0xffff0000, v197
	v_lshlrev_b32_e32 v196, 16, v198
	v_and_b32_e32 v197, 0xffff0000, v198
	v_lshlrev_b32_e32 v198, 16, v199
	v_and_b32_e32 v199, 0xffff0000, v199
	v_max_f32_e32 v192, 0x1e3ce508, v192
	v_max_f32_e32 v193, 0x1e3ce508, v193
	v_max_f32_e32 v194, 0x1e3ce508, v194
	v_max_f32_e32 v195, 0x1e3ce508, v195
	v_max_f32_e32 v196, 0x1e3ce508, v196
	v_max_f32_e32 v197, 0x1e3ce508, v197
	v_max_f32_e32 v198, 0x1e3ce508, v198
	v_max_f32_e32 v199, 0x1e3ce508, v199
	v_rcp_f32_e32 v192, v192
	v_rcp_f32_e32 v193, v193
	v_rcp_f32_e32 v194, v194
	v_rcp_f32_e32 v195, v195
	v_rcp_f32_e32 v196, v196
	v_rcp_f32_e32 v197, v197
	v_rcp_f32_e32 v198, v198
	v_rcp_f32_e32 v199, v199
	v_pk_mul_f32 v[168:169], v[168:169], v[192:193]
	v_pk_mul_f32 v[170:171], v[170:171], v[194:195]
	v_pk_mul_f32 v[224:225], v[224:225], v[196:197]
	v_pk_mul_f32 v[226:227], v[226:227], v[198:199]
	v_pk_mul_f32 v[64:65], v[64:65], v[168:169]
	v_pk_mul_f32 v[66:67], v[66:67], v[170:171]
	v_pk_mul_f32 v[60:61], v[60:61], v[224:225]
	v_pk_mul_f32 v[62:63], v[62:63], v[226:227]
	s_add_u32 s28, s26, 0xf0000
	s_addc_u32 s29, s27, 0
	global_load_dwordx4 v[184:187], v191, s[28:29]
	global_load_dwordx4 v[192:195], v191, s[28:29] offset:2048
	s_waitcnt vmcnt(12)
	v_lshlrev_b32_e32 v168, 16, v212
	v_and_b32_e32 v169, 0xffff0000, v212
	v_lshlrev_b32_e32 v170, 16, v213
	v_and_b32_e32 v171, 0xffff0000, v213
	v_lshlrev_b32_e32 v224, 16, v214
	v_and_b32_e32 v225, 0xffff0000, v214
	v_lshlrev_b32_e32 v226, 16, v215
	v_and_b32_e32 v227, 0xffff0000, v215
	v_max_f32_e32 v168, 0x1e3ce508, v168
	v_max_f32_e32 v169, 0x1e3ce508, v169
	v_max_f32_e32 v170, 0x1e3ce508, v170
	v_max_f32_e32 v171, 0x1e3ce508, v171
	v_max_f32_e32 v224, 0x1e3ce508, v224
	v_max_f32_e32 v225, 0x1e3ce508, v225
	v_max_f32_e32 v226, 0x1e3ce508, v226
	v_max_f32_e32 v227, 0x1e3ce508, v227
	v_lshlrev_b32_e32 v212, 16, v216
	v_and_b32_e32 v213, 0xffff0000, v216
	v_lshlrev_b32_e32 v214, 16, v217
	v_and_b32_e32 v215, 0xffff0000, v217
	v_lshlrev_b32_e32 v216, 16, v218
	v_and_b32_e32 v217, 0xffff0000, v218
	v_lshlrev_b32_e32 v218, 16, v219
	v_and_b32_e32 v219, 0xffff0000, v219
	v_max_f32_e32 v212, 0x1e3ce508, v212
	v_max_f32_e32 v213, 0x1e3ce508, v213
	v_max_f32_e32 v214, 0x1e3ce508, v214
	v_max_f32_e32 v215, 0x1e3ce508, v215
	v_max_f32_e32 v216, 0x1e3ce508, v216
	v_max_f32_e32 v217, 0x1e3ce508, v217
	v_max_f32_e32 v218, 0x1e3ce508, v218
	v_max_f32_e32 v219, 0x1e3ce508, v219
	v_rcp_f32_e32 v212, v212
	v_rcp_f32_e32 v213, v213
	v_rcp_f32_e32 v214, v214
	v_rcp_f32_e32 v215, v215
	v_rcp_f32_e32 v216, v216
	v_rcp_f32_e32 v217, v217
	v_rcp_f32_e32 v218, v218
	v_rcp_f32_e32 v219, v219
	v_pk_mul_f32 v[168:169], v[168:169], v[212:213]
	v_pk_mul_f32 v[170:171], v[170:171], v[214:215]
	v_pk_mul_f32 v[224:225], v[224:225], v[216:217]
	v_pk_mul_f32 v[226:227], v[226:227], v[218:219]
	v_pk_mul_f32 v[88:89], v[88:89], v[168:169]
	v_pk_mul_f32 v[90:91], v[90:91], v[170:171]
	v_pk_mul_f32 v[84:85], v[84:85], v[224:225]
	v_pk_mul_f32 v[86:87], v[86:87], v[226:227]
	s_add_u32 s28, s26, 0xf0000
	s_addc_u32 s29, s27, 0
	global_load_dwordx4 v[196:199], v191, s[28:29] offset:256
	global_load_dwordx4 v[212:215], v191, s[28:29] offset:2304
	s_waitcnt vmcnt(12)
	v_lshlrev_b32_e32 v168, 16, v220
	v_and_b32_e32 v169, 0xffff0000, v220
	v_lshlrev_b32_e32 v170, 16, v221
	v_and_b32_e32 v171, 0xffff0000, v221
	v_lshlrev_b32_e32 v224, 16, v222
	v_and_b32_e32 v225, 0xffff0000, v222
	v_lshlrev_b32_e32 v226, 16, v223
	v_and_b32_e32 v227, 0xffff0000, v223
	v_max_f32_e32 v168, 0x1e3ce508, v168
	v_max_f32_e32 v169, 0x1e3ce508, v169
	v_max_f32_e32 v170, 0x1e3ce508, v170
	v_max_f32_e32 v171, 0x1e3ce508, v171
	v_max_f32_e32 v224, 0x1e3ce508, v224
	v_max_f32_e32 v225, 0x1e3ce508, v225
	v_max_f32_e32 v226, 0x1e3ce508, v226
	v_max_f32_e32 v227, 0x1e3ce508, v227
	v_lshlrev_b32_e32 v220, 16, v132
	v_and_b32_e32 v221, 0xffff0000, v132
	v_lshlrev_b32_e32 v222, 16, v133
	v_and_b32_e32 v223, 0xffff0000, v133
	v_lshlrev_b32_e32 v132, 16, v134
	v_and_b32_e32 v133, 0xffff0000, v134
	v_lshlrev_b32_e32 v134, 16, v135
	v_and_b32_e32 v135, 0xffff0000, v135
	v_max_f32_e32 v220, 0x1e3ce508, v220
	v_max_f32_e32 v221, 0x1e3ce508, v221
	v_max_f32_e32 v222, 0x1e3ce508, v222
	v_max_f32_e32 v223, 0x1e3ce508, v223
	v_max_f32_e32 v132, 0x1e3ce508, v132
	v_max_f32_e32 v133, 0x1e3ce508, v133
	v_max_f32_e32 v134, 0x1e3ce508, v134
	v_max_f32_e32 v135, 0x1e3ce508, v135
	v_rcp_f32_e32 v220, v220
	v_rcp_f32_e32 v221, v221
	v_rcp_f32_e32 v222, v222
	v_rcp_f32_e32 v223, v223
	v_rcp_f32_e32 v132, v132
	v_rcp_f32_e32 v133, v133
	v_rcp_f32_e32 v134, v134
	v_rcp_f32_e32 v135, v135
	v_pk_mul_f32 v[168:169], v[168:169], v[220:221]
	v_pk_mul_f32 v[170:171], v[170:171], v[222:223]
	v_pk_mul_f32 v[224:225], v[224:225], v[132:133]
	v_pk_mul_f32 v[226:227], v[226:227], v[134:135]
	v_pk_mul_f32 v[56:57], v[56:57], v[168:169]
	v_pk_mul_f32 v[58:59], v[58:59], v[170:171]
	v_pk_mul_f32 v[48:49], v[48:49], v[224:225]
	v_pk_mul_f32 v[50:51], v[50:51], v[226:227]
	s_add_u32 s28, s26, 0x108000
	s_addc_u32 s29, s27, 0
	global_load_dwordx4 v[216:219], v191, s[28:29]
	global_load_dwordx4 v[220:223], v191, s[28:29] offset:2048
	s_waitcnt vmcnt(12)
	v_lshlrev_b32_e32 v168, 16, v136
	v_and_b32_e32 v169, 0xffff0000, v136
	v_lshlrev_b32_e32 v170, 16, v137
	v_and_b32_e32 v171, 0xffff0000, v137
	v_lshlrev_b32_e32 v224, 16, v138
	v_and_b32_e32 v225, 0xffff0000, v138
	v_lshlrev_b32_e32 v226, 16, v139
	v_and_b32_e32 v227, 0xffff0000, v139
	v_max_f32_e32 v168, 0x1e3ce508, v168
	v_max_f32_e32 v169, 0x1e3ce508, v169
	v_max_f32_e32 v170, 0x1e3ce508, v170
	v_max_f32_e32 v171, 0x1e3ce508, v171
	v_max_f32_e32 v224, 0x1e3ce508, v224
	v_max_f32_e32 v225, 0x1e3ce508, v225
	v_max_f32_e32 v226, 0x1e3ce508, v226
	v_max_f32_e32 v227, 0x1e3ce508, v227
	v_lshlrev_b32_e32 v136, 16, v140
	v_and_b32_e32 v137, 0xffff0000, v140
	v_lshlrev_b32_e32 v138, 16, v141
	v_and_b32_e32 v139, 0xffff0000, v141
	v_lshlrev_b32_e32 v140, 16, v142
	v_and_b32_e32 v141, 0xffff0000, v142
	v_lshlrev_b32_e32 v142, 16, v143
	v_and_b32_e32 v143, 0xffff0000, v143
	v_max_f32_e32 v136, 0x1e3ce508, v136
	v_max_f32_e32 v137, 0x1e3ce508, v137
	v_max_f32_e32 v138, 0x1e3ce508, v138
	v_max_f32_e32 v139, 0x1e3ce508, v139
	v_max_f32_e32 v140, 0x1e3ce508, v140
	v_max_f32_e32 v141, 0x1e3ce508, v141
	v_max_f32_e32 v142, 0x1e3ce508, v142
	v_max_f32_e32 v143, 0x1e3ce508, v143
	v_rcp_f32_e32 v136, v136
	v_rcp_f32_e32 v137, v137
	v_rcp_f32_e32 v138, v138
	v_rcp_f32_e32 v139, v139
	v_rcp_f32_e32 v140, v140
	v_rcp_f32_e32 v141, v141
	v_rcp_f32_e32 v142, v142
	v_rcp_f32_e32 v143, v143
	v_pk_mul_f32 v[168:169], v[168:169], v[136:137]
	v_pk_mul_f32 v[170:171], v[170:171], v[138:139]
	v_pk_mul_f32 v[224:225], v[224:225], v[140:141]
	v_pk_mul_f32 v[226:227], v[226:227], v[142:143]
	v_pk_mul_f32 v[52:53], v[52:53], v[168:169]
	v_pk_mul_f32 v[54:55], v[54:55], v[170:171]
	v_pk_mul_f32 v[44:45], v[44:45], v[224:225]
	v_pk_mul_f32 v[46:47], v[46:47], v[226:227]
	s_add_u32 s28, s26, 0x108000
	s_addc_u32 s29, s27, 0
	global_load_dwordx4 v[132:135], v191, s[28:29] offset:256
	global_load_dwordx4 v[136:139], v191, s[28:29] offset:2304
	s_waitcnt vmcnt(12)
	v_lshlrev_b32_e32 v168, 16, v144
	v_and_b32_e32 v169, 0xffff0000, v144
	v_lshlrev_b32_e32 v170, 16, v145
	v_and_b32_e32 v171, 0xffff0000, v145
	v_lshlrev_b32_e32 v224, 16, v146
	v_and_b32_e32 v225, 0xffff0000, v146
	v_lshlrev_b32_e32 v226, 16, v147
	v_and_b32_e32 v227, 0xffff0000, v147
	v_max_f32_e32 v168, 0x1e3ce508, v168
	v_max_f32_e32 v169, 0x1e3ce508, v169
	v_max_f32_e32 v170, 0x1e3ce508, v170
	v_max_f32_e32 v171, 0x1e3ce508, v171
	v_max_f32_e32 v224, 0x1e3ce508, v224
	v_max_f32_e32 v225, 0x1e3ce508, v225
	v_max_f32_e32 v226, 0x1e3ce508, v226
	v_max_f32_e32 v227, 0x1e3ce508, v227
	v_lshlrev_b32_e32 v144, 16, v148
	v_and_b32_e32 v145, 0xffff0000, v148
	v_lshlrev_b32_e32 v146, 16, v149
	v_and_b32_e32 v147, 0xffff0000, v149
	v_lshlrev_b32_e32 v148, 16, v150
	v_and_b32_e32 v149, 0xffff0000, v150
	v_lshlrev_b32_e32 v150, 16, v151
	v_and_b32_e32 v151, 0xffff0000, v151
	v_max_f32_e32 v144, 0x1e3ce508, v144
	v_max_f32_e32 v145, 0x1e3ce508, v145
	v_max_f32_e32 v146, 0x1e3ce508, v146
	v_max_f32_e32 v147, 0x1e3ce508, v147
	v_max_f32_e32 v148, 0x1e3ce508, v148
	v_max_f32_e32 v149, 0x1e3ce508, v149
	v_max_f32_e32 v150, 0x1e3ce508, v150
	v_max_f32_e32 v151, 0x1e3ce508, v151
	v_rcp_f32_e32 v144, v144
	v_rcp_f32_e32 v145, v145
	v_rcp_f32_e32 v146, v146
	v_rcp_f32_e32 v147, v147
	v_rcp_f32_e32 v148, v148
	v_rcp_f32_e32 v149, v149
	v_rcp_f32_e32 v150, v150
	v_rcp_f32_e32 v151, v151
	v_pk_mul_f32 v[168:169], v[168:169], v[144:145]
	v_pk_mul_f32 v[170:171], v[170:171], v[146:147]
	v_pk_mul_f32 v[224:225], v[224:225], v[148:149]
	v_pk_mul_f32 v[226:227], v[226:227], v[150:151]
	v_pk_mul_f32 v[16:17], v[16:17], v[168:169]
	v_pk_mul_f32 v[18:19], v[18:19], v[170:171]
	v_pk_mul_f32 v[12:13], v[12:13], v[224:225]
	v_pk_mul_f32 v[14:15], v[14:15], v[226:227]
	s_waitcnt vmcnt(10)
	v_lshlrev_b32_e32 v168, 16, v152
	v_and_b32_e32 v169, 0xffff0000, v152
	v_lshlrev_b32_e32 v170, 16, v153
	v_and_b32_e32 v171, 0xffff0000, v153
	v_lshlrev_b32_e32 v224, 16, v154
	v_and_b32_e32 v225, 0xffff0000, v154
	v_lshlrev_b32_e32 v226, 16, v155
	v_and_b32_e32 v227, 0xffff0000, v155
	v_max_f32_e32 v168, 0x1e3ce508, v168
	v_max_f32_e32 v169, 0x1e3ce508, v169
	v_max_f32_e32 v170, 0x1e3ce508, v170
	v_max_f32_e32 v171, 0x1e3ce508, v171
	v_max_f32_e32 v224, 0x1e3ce508, v224
	v_max_f32_e32 v225, 0x1e3ce508, v225
	v_max_f32_e32 v226, 0x1e3ce508, v226
	v_max_f32_e32 v227, 0x1e3ce508, v227
	v_lshlrev_b32_e32 v152, 16, v156
	v_and_b32_e32 v153, 0xffff0000, v156
	v_lshlrev_b32_e32 v154, 16, v157
	v_and_b32_e32 v155, 0xffff0000, v157
	v_lshlrev_b32_e32 v156, 16, v158
	v_and_b32_e32 v157, 0xffff0000, v158
	v_lshlrev_b32_e32 v158, 16, v159
	v_and_b32_e32 v159, 0xffff0000, v159
	v_max_f32_e32 v152, 0x1e3ce508, v152
	v_max_f32_e32 v153, 0x1e3ce508, v153
	v_max_f32_e32 v154, 0x1e3ce508, v154
	v_max_f32_e32 v155, 0x1e3ce508, v155
	v_max_f32_e32 v156, 0x1e3ce508, v156
	v_max_f32_e32 v157, 0x1e3ce508, v157
	v_max_f32_e32 v158, 0x1e3ce508, v158
	v_max_f32_e32 v159, 0x1e3ce508, v159
	v_rcp_f32_e32 v152, v152
	v_rcp_f32_e32 v153, v153
	v_rcp_f32_e32 v154, v154
	v_rcp_f32_e32 v155, v155
	v_rcp_f32_e32 v156, v156
	v_rcp_f32_e32 v157, v157
	v_rcp_f32_e32 v158, v158
	v_rcp_f32_e32 v159, v159
	v_pk_mul_f32 v[168:169], v[168:169], v[152:153]
	v_pk_mul_f32 v[170:171], v[170:171], v[154:155]
	v_pk_mul_f32 v[224:225], v[224:225], v[156:157]
	v_pk_mul_f32 v[226:227], v[226:227], v[158:159]
	v_pk_mul_f32 v[40:41], v[40:41], v[168:169]
	v_pk_mul_f32 v[42:43], v[42:43], v[170:171]
	v_pk_mul_f32 v[36:37], v[36:37], v[224:225]
	v_pk_mul_f32 v[38:39], v[38:39], v[226:227]
	s_waitcnt vmcnt(8)
	v_lshlrev_b32_e32 v168, 16, v160
	v_and_b32_e32 v169, 0xffff0000, v160
	v_lshlrev_b32_e32 v170, 16, v161
	v_and_b32_e32 v171, 0xffff0000, v161
	v_lshlrev_b32_e32 v224, 16, v162
	v_and_b32_e32 v225, 0xffff0000, v162
	v_lshlrev_b32_e32 v226, 16, v163
	v_and_b32_e32 v227, 0xffff0000, v163
	v_max_f32_e32 v168, 0x1e3ce508, v168
	v_max_f32_e32 v169, 0x1e3ce508, v169
	v_max_f32_e32 v170, 0x1e3ce508, v170
	v_max_f32_e32 v171, 0x1e3ce508, v171
	v_max_f32_e32 v224, 0x1e3ce508, v224
	v_max_f32_e32 v225, 0x1e3ce508, v225
	v_max_f32_e32 v226, 0x1e3ce508, v226
	v_max_f32_e32 v227, 0x1e3ce508, v227
	v_lshlrev_b32_e32 v160, 16, v180
	v_and_b32_e32 v161, 0xffff0000, v180
	v_lshlrev_b32_e32 v162, 16, v181
	v_and_b32_e32 v163, 0xffff0000, v181
	v_lshlrev_b32_e32 v180, 16, v182
	v_and_b32_e32 v181, 0xffff0000, v182
	v_lshlrev_b32_e32 v182, 16, v183
	v_and_b32_e32 v183, 0xffff0000, v183
	v_max_f32_e32 v160, 0x1e3ce508, v160
	v_max_f32_e32 v161, 0x1e3ce508, v161
	v_max_f32_e32 v162, 0x1e3ce508, v162
	v_max_f32_e32 v163, 0x1e3ce508, v163
	v_max_f32_e32 v180, 0x1e3ce508, v180
	v_max_f32_e32 v181, 0x1e3ce508, v181
	v_max_f32_e32 v182, 0x1e3ce508, v182
	v_max_f32_e32 v183, 0x1e3ce508, v183
	v_rcp_f32_e32 v160, v160
	v_rcp_f32_e32 v161, v161
	v_rcp_f32_e32 v162, v162
	v_rcp_f32_e32 v163, v163
	v_rcp_f32_e32 v180, v180
	v_rcp_f32_e32 v181, v181
	v_rcp_f32_e32 v182, v182
	v_rcp_f32_e32 v183, v183
	v_pk_mul_f32 v[168:169], v[168:169], v[160:161]
	v_pk_mul_f32 v[170:171], v[170:171], v[162:163]
	v_pk_mul_f32 v[224:225], v[224:225], v[180:181]
	v_pk_mul_f32 v[226:227], v[226:227], v[182:183]
	v_pk_mul_f32 v[8:9], v[8:9], v[168:169]
	v_pk_mul_f32 v[10:11], v[10:11], v[170:171]
	v_pk_mul_f32 v[4:5], v[4:5], v[224:225]
	v_pk_mul_f32 v[6:7], v[6:7], v[226:227]
	s_waitcnt vmcnt(6)
	v_lshlrev_b32_e32 v168, 16, v184
	v_and_b32_e32 v169, 0xffff0000, v184
	v_lshlrev_b32_e32 v170, 16, v185
	v_and_b32_e32 v171, 0xffff0000, v185
	v_lshlrev_b32_e32 v224, 16, v186
	v_and_b32_e32 v225, 0xffff0000, v186
	v_lshlrev_b32_e32 v226, 16, v187
	v_and_b32_e32 v227, 0xffff0000, v187
	v_max_f32_e32 v168, 0x1e3ce508, v168
	v_max_f32_e32 v169, 0x1e3ce508, v169
	v_max_f32_e32 v170, 0x1e3ce508, v170
	v_max_f32_e32 v171, 0x1e3ce508, v171
	v_max_f32_e32 v224, 0x1e3ce508, v224
	v_max_f32_e32 v225, 0x1e3ce508, v225
	v_max_f32_e32 v226, 0x1e3ce508, v226
	v_max_f32_e32 v227, 0x1e3ce508, v227
	v_lshlrev_b32_e32 v184, 16, v192
	v_and_b32_e32 v185, 0xffff0000, v192
	v_lshlrev_b32_e32 v186, 16, v193
	v_and_b32_e32 v187, 0xffff0000, v193
	v_lshlrev_b32_e32 v192, 16, v194
	v_and_b32_e32 v193, 0xffff0000, v194
	v_lshlrev_b32_e32 v194, 16, v195
	v_and_b32_e32 v195, 0xffff0000, v195
	v_max_f32_e32 v184, 0x1e3ce508, v184
	v_max_f32_e32 v185, 0x1e3ce508, v185
	v_max_f32_e32 v186, 0x1e3ce508, v186
	v_max_f32_e32 v187, 0x1e3ce508, v187
	v_max_f32_e32 v192, 0x1e3ce508, v192
	v_max_f32_e32 v193, 0x1e3ce508, v193
	v_max_f32_e32 v194, 0x1e3ce508, v194
	v_max_f32_e32 v195, 0x1e3ce508, v195
	v_rcp_f32_e32 v184, v184
	v_rcp_f32_e32 v185, v185
	v_rcp_f32_e32 v186, v186
	v_rcp_f32_e32 v187, v187
	v_rcp_f32_e32 v192, v192
	v_rcp_f32_e32 v193, v193
	v_rcp_f32_e32 v194, v194
	v_rcp_f32_e32 v195, v195
	v_pk_mul_f32 v[168:169], v[168:169], v[184:185]
	v_pk_mul_f32 v[170:171], v[170:171], v[186:187]
	v_pk_mul_f32 v[224:225], v[224:225], v[192:193]
	v_pk_mul_f32 v[226:227], v[226:227], v[194:195]
	v_pk_mul_f32 v[32:33], v[32:33], v[168:169]
	v_pk_mul_f32 v[34:35], v[34:35], v[170:171]
	v_pk_mul_f32 v[28:29], v[28:29], v[224:225]
	v_pk_mul_f32 v[30:31], v[30:31], v[226:227]
	s_waitcnt vmcnt(4)
	v_lshlrev_b32_e32 v168, 16, v196
	v_and_b32_e32 v169, 0xffff0000, v196
	v_lshlrev_b32_e32 v170, 16, v197
	v_and_b32_e32 v171, 0xffff0000, v197
	v_lshlrev_b32_e32 v224, 16, v198
	v_and_b32_e32 v225, 0xffff0000, v198
	v_lshlrev_b32_e32 v226, 16, v199
	v_and_b32_e32 v227, 0xffff0000, v199
	v_max_f32_e32 v168, 0x1e3ce508, v168
	v_max_f32_e32 v169, 0x1e3ce508, v169
	v_max_f32_e32 v170, 0x1e3ce508, v170
	v_max_f32_e32 v171, 0x1e3ce508, v171
	v_max_f32_e32 v224, 0x1e3ce508, v224
	v_max_f32_e32 v225, 0x1e3ce508, v225
	v_max_f32_e32 v226, 0x1e3ce508, v226
	v_max_f32_e32 v227, 0x1e3ce508, v227
	v_lshlrev_b32_e32 v196, 16, v212
	v_and_b32_e32 v197, 0xffff0000, v212
	v_lshlrev_b32_e32 v198, 16, v213
	v_and_b32_e32 v199, 0xffff0000, v213
	v_lshlrev_b32_e32 v212, 16, v214
	v_and_b32_e32 v213, 0xffff0000, v214
	v_lshlrev_b32_e32 v214, 16, v215
	v_and_b32_e32 v215, 0xffff0000, v215
	v_max_f32_e32 v196, 0x1e3ce508, v196
	v_max_f32_e32 v197, 0x1e3ce508, v197
	v_max_f32_e32 v198, 0x1e3ce508, v198
	v_max_f32_e32 v199, 0x1e3ce508, v199
	v_max_f32_e32 v212, 0x1e3ce508, v212
	v_max_f32_e32 v213, 0x1e3ce508, v213
	v_max_f32_e32 v214, 0x1e3ce508, v214
	v_max_f32_e32 v215, 0x1e3ce508, v215
	v_rcp_f32_e32 v196, v196
	v_rcp_f32_e32 v197, v197
	v_rcp_f32_e32 v198, v198
	v_rcp_f32_e32 v199, v199
	v_rcp_f32_e32 v212, v212
	v_rcp_f32_e32 v213, v213
	v_rcp_f32_e32 v214, v214
	v_rcp_f32_e32 v215, v215
	v_pk_mul_f32 v[168:169], v[168:169], v[196:197]
	v_pk_mul_f32 v[170:171], v[170:171], v[198:199]
	v_pk_mul_f32 v[224:225], v[224:225], v[212:213]
	v_pk_mul_f32 v[226:227], v[226:227], v[214:215]
	v_pk_mul_f32 v[116:117], v[116:117], v[168:169]
	v_pk_mul_f32 v[118:119], v[118:119], v[170:171]
	v_pk_mul_f32 v[120:121], v[120:121], v[224:225]
	v_pk_mul_f32 v[122:123], v[122:123], v[226:227]
	s_waitcnt vmcnt(2)
	v_lshlrev_b32_e32 v168, 16, v216
	v_and_b32_e32 v169, 0xffff0000, v216
	v_lshlrev_b32_e32 v170, 16, v217
	v_and_b32_e32 v171, 0xffff0000, v217
	v_lshlrev_b32_e32 v224, 16, v218
	v_and_b32_e32 v225, 0xffff0000, v218
	v_lshlrev_b32_e32 v226, 16, v219
	v_and_b32_e32 v227, 0xffff0000, v219
	v_max_f32_e32 v168, 0x1e3ce508, v168
	v_max_f32_e32 v169, 0x1e3ce508, v169
	v_max_f32_e32 v170, 0x1e3ce508, v170
	v_max_f32_e32 v171, 0x1e3ce508, v171
	v_max_f32_e32 v224, 0x1e3ce508, v224
	v_max_f32_e32 v225, 0x1e3ce508, v225
	v_max_f32_e32 v226, 0x1e3ce508, v226
	v_max_f32_e32 v227, 0x1e3ce508, v227
	v_lshlrev_b32_e32 v216, 16, v220
	v_and_b32_e32 v217, 0xffff0000, v220
	v_lshlrev_b32_e32 v218, 16, v221
	v_and_b32_e32 v219, 0xffff0000, v221
	v_lshlrev_b32_e32 v220, 16, v222
	v_and_b32_e32 v221, 0xffff0000, v222
	v_lshlrev_b32_e32 v222, 16, v223
	v_and_b32_e32 v223, 0xffff0000, v223
	v_max_f32_e32 v216, 0x1e3ce508, v216
	v_max_f32_e32 v217, 0x1e3ce508, v217
	v_max_f32_e32 v218, 0x1e3ce508, v218
	v_max_f32_e32 v219, 0x1e3ce508, v219
	v_max_f32_e32 v220, 0x1e3ce508, v220
	v_max_f32_e32 v221, 0x1e3ce508, v221
	v_max_f32_e32 v222, 0x1e3ce508, v222
	v_max_f32_e32 v223, 0x1e3ce508, v223
	v_rcp_f32_e32 v216, v216
	v_rcp_f32_e32 v217, v217
	v_rcp_f32_e32 v218, v218
	v_rcp_f32_e32 v219, v219
	v_rcp_f32_e32 v220, v220
	v_rcp_f32_e32 v221, v221
	v_rcp_f32_e32 v222, v222
	v_rcp_f32_e32 v223, v223
	v_pk_mul_f32 v[168:169], v[168:169], v[216:217]
	v_pk_mul_f32 v[170:171], v[170:171], v[218:219]
	v_pk_mul_f32 v[224:225], v[224:225], v[220:221]
	v_pk_mul_f32 v[226:227], v[226:227], v[222:223]
	v_pk_mul_f32 v[24:25], v[24:25], v[168:169]
	v_pk_mul_f32 v[26:27], v[26:27], v[170:171]
	v_pk_mul_f32 v[20:21], v[20:21], v[224:225]
	v_pk_mul_f32 v[22:23], v[22:23], v[226:227]
	s_waitcnt vmcnt(0)
	v_lshlrev_b32_e32 v168, 16, v132
	v_and_b32_e32 v169, 0xffff0000, v132
	v_lshlrev_b32_e32 v170, 16, v133
	v_and_b32_e32 v171, 0xffff0000, v133
	v_lshlrev_b32_e32 v224, 16, v134
	v_and_b32_e32 v225, 0xffff0000, v134
	v_lshlrev_b32_e32 v226, 16, v135
	v_and_b32_e32 v227, 0xffff0000, v135
	v_max_f32_e32 v168, 0x1e3ce508, v168
	v_max_f32_e32 v169, 0x1e3ce508, v169
	v_max_f32_e32 v170, 0x1e3ce508, v170
	v_max_f32_e32 v171, 0x1e3ce508, v171
	v_max_f32_e32 v224, 0x1e3ce508, v224
	v_max_f32_e32 v225, 0x1e3ce508, v225
	v_max_f32_e32 v226, 0x1e3ce508, v226
	v_max_f32_e32 v227, 0x1e3ce508, v227
	v_lshlrev_b32_e32 v132, 16, v136
	v_and_b32_e32 v133, 0xffff0000, v136
	v_lshlrev_b32_e32 v134, 16, v137
	v_and_b32_e32 v135, 0xffff0000, v137
	v_lshlrev_b32_e32 v136, 16, v138
	v_and_b32_e32 v137, 0xffff0000, v138
	v_lshlrev_b32_e32 v138, 16, v139
	v_and_b32_e32 v139, 0xffff0000, v139
	v_max_f32_e32 v132, 0x1e3ce508, v132
	v_max_f32_e32 v133, 0x1e3ce508, v133
	v_max_f32_e32 v134, 0x1e3ce508, v134
	v_max_f32_e32 v135, 0x1e3ce508, v135
	v_max_f32_e32 v136, 0x1e3ce508, v136
	v_max_f32_e32 v137, 0x1e3ce508, v137
	v_max_f32_e32 v138, 0x1e3ce508, v138
	v_max_f32_e32 v139, 0x1e3ce508, v139
	v_rcp_f32_e32 v132, v132
	v_rcp_f32_e32 v133, v133
	v_rcp_f32_e32 v134, v134
	v_rcp_f32_e32 v135, v135
	v_rcp_f32_e32 v136, v136
	v_rcp_f32_e32 v137, v137
	v_rcp_f32_e32 v138, v138
	v_rcp_f32_e32 v139, v139
	v_pk_mul_f32 v[168:169], v[168:169], v[132:133]
	v_pk_mul_f32 v[170:171], v[170:171], v[134:135]
	v_pk_mul_f32 v[224:225], v[224:225], v[136:137]
	v_pk_mul_f32 v[226:227], v[226:227], v[138:139]
	v_pk_mul_f32 v[124:125], v[124:125], v[168:169]
	v_pk_mul_f32 v[126:127], v[126:127], v[170:171]
	v_pk_mul_f32 v[128:129], v[128:129], v[224:225]
	v_pk_mul_f32 v[130:131], v[130:131], v[226:227]
	s_branch .Lmg_done
.Lmg_last:
	s_add_u32 s28, s26, 0x48000
	s_addc_u32 s29, s27, 0
	global_load_dwordx4 v[132:135], v191, s[28:29]
	s_add_u32 s28, s26, 0x48000
	s_addc_u32 s29, s27, 0
	global_load_dwordx4 v[136:139], v191, s[28:29] offset:256
	s_add_u32 s28, s26, 0xc0000
	s_addc_u32 s29, s27, 0
	global_load_dwordx4 v[140:143], v191, s[28:29]
	s_add_u32 s28, s26, 0xc0000
	s_addc_u32 s29, s27, 0
	global_load_dwordx4 v[144:147], v191, s[28:29] offset:256
	s_add_u32 s28, s26, 0xd8000
	s_addc_u32 s29, s27, 0
	global_load_dwordx4 v[148:151], v191, s[28:29]
	s_add_u32 s28, s26, 0xd8000
	s_addc_u32 s29, s27, 0
	global_load_dwordx4 v[152:155], v191, s[28:29] offset:256
	s_add_u32 s28, s26, 0xf0000
	s_addc_u32 s29, s27, 0
	global_load_dwordx4 v[156:159], v191, s[28:29]
	s_add_u32 s28, s26, 0xf0000
	s_addc_u32 s29, s27, 0
	global_load_dwordx4 v[160:163], v191, s[28:29] offset:256
	s_add_u32 s28, s26, 0x108000
	s_addc_u32 s29, s27, 0
	global_load_dwordx4 v[180:183], v191, s[28:29]
	s_add_u32 s28, s26, 0x108000
	s_addc_u32 s29, s27, 0
	global_load_dwordx4 v[184:187], v191, s[28:29] offset:256
	s_and_b64 vcc, exec, s[20:21]
	s_cbranch_vccz .Lmg_nbb
	s_barrier
.Lmg_nbb:
	v_lshlrev_b32_e32 v168, 16, v228
	v_and_b32_e32 v169, 0xffff0000, v228
	v_lshlrev_b32_e32 v170, 16, v229
	v_and_b32_e32 v171, 0xffff0000, v229
	v_lshlrev_b32_e32 v224, 16, v230
	v_and_b32_e32 v225, 0xffff0000, v230
	v_lshlrev_b32_e32 v226, 16, v231
	v_and_b32_e32 v227, 0xffff0000, v231
	v_max_f32_e32 v168, 0x1e3ce508, v168
	v_max_f32_e32 v169, 0x1e3ce508, v169
	v_max_f32_e32 v170, 0x1e3ce508, v170
	v_max_f32_e32 v171, 0x1e3ce508, v171
	v_max_f32_e32 v224, 0x1e3ce508, v224
	v_max_f32_e32 v225, 0x1e3ce508, v225
	v_max_f32_e32 v226, 0x1e3ce508, v226
	v_max_f32_e32 v227, 0x1e3ce508, v227
	v_pk_mul_f32 v[112:113], v[112:113], v[168:169]
	v_pk_mul_f32 v[114:115], v[114:115], v[170:171]
	v_pk_mul_f32 v[108:109], v[108:109], v[224:225]
	v_pk_mul_f32 v[110:111], v[110:111], v[226:227]
	v_cvt_pk_bf16_f32 v228, v112, v113
	v_cvt_pk_bf16_f32 v229, v114, v115
	v_cvt_pk_bf16_f32 v230, v108, v109
	v_cvt_pk_bf16_f32 v231, v110, v111
	v_lshlrev_b32_e32 v168, 16, v232
	v_and_b32_e32 v169, 0xffff0000, v232
	v_lshlrev_b32_e32 v170, 16, v233
	v_and_b32_e32 v171, 0xffff0000, v233
	v_lshlrev_b32_e32 v224, 16, v234
	v_and_b32_e32 v225, 0xffff0000, v234
	v_lshlrev_b32_e32 v226, 16, v235
	v_and_b32_e32 v227, 0xffff0000, v235
	v_max_f32_e32 v168, 0x1e3ce508, v168
	v_max_f32_e32 v169, 0x1e3ce508, v169
	v_max_f32_e32 v170, 0x1e3ce508, v170
	v_max_f32_e32 v171, 0x1e3ce508, v171
	v_max_f32_e32 v224, 0x1e3ce508, v224
	v_max_f32_e32 v225, 0x1e3ce508, v225
	v_max_f32_e32 v226, 0x1e3ce508, v226
	v_max_f32_e32 v227, 0x1e3ce508, v227
	v_pk_mul_f32 v[80:81], v[80:81], v[168:169]
	v_pk_mul_f32 v[82:83], v[82:83], v[170:171]
	v_pk_mul_f32 v[76:77], v[76:77], v[224:225]
	v_pk_mul_f32 v[78:79], v[78:79], v[226:227]
	v_cvt_pk_bf16_f32 v232, v80, v81
	v_cvt_pk_bf16_f32 v233, v82, v83
	v_cvt_pk_bf16_f32 v234, v76, v77
	v_cvt_pk_bf16_f32 v235, v78, v79
	v_lshlrev_b32_e32 v168, 16, v236
	v_and_b32_e32 v169, 0xffff0000, v236
	v_lshlrev_b32_e32 v170, 16, v237
	v_and_b32_e32 v171, 0xffff0000, v237
	v_lshlrev_b32_e32 v224, 16, v238
	v_and_b32_e32 v225, 0xffff0000, v238
	v_lshlrev_b32_e32 v226, 16, v239
	v_and_b32_e32 v227, 0xffff0000, v239
	v_max_f32_e32 v168, 0x1e3ce508, v168
	v_max_f32_e32 v169, 0x1e3ce508, v169
	v_max_f32_e32 v170, 0x1e3ce508, v170
	v_max_f32_e32 v171, 0x1e3ce508, v171
	v_max_f32_e32 v224, 0x1e3ce508, v224
	v_max_f32_e32 v225, 0x1e3ce508, v225
	v_max_f32_e32 v226, 0x1e3ce508, v226
	v_max_f32_e32 v227, 0x1e3ce508, v227
	v_pk_mul_f32 v[104:105], v[104:105], v[168:169]
	v_pk_mul_f32 v[106:107], v[106:107], v[170:171]
	v_pk_mul_f32 v[100:101], v[100:101], v[224:225]
	v_pk_mul_f32 v[102:103], v[102:103], v[226:227]
	v_cvt_pk_bf16_f32 v236, v104, v105
	v_cvt_pk_bf16_f32 v237, v106, v107
	v_cvt_pk_bf16_f32 v238, v100, v101
	v_cvt_pk_bf16_f32 v239, v102, v103
	v_lshlrev_b32_e32 v168, 16, v240
	v_and_b32_e32 v169, 0xffff0000, v240
	v_lshlrev_b32_e32 v170, 16, v241
	v_and_b32_e32 v171, 0xffff0000, v241
	v_lshlrev_b32_e32 v224, 16, v242
	v_and_b32_e32 v225, 0xffff0000, v242
	v_lshlrev_b32_e32 v226, 16, v243
	v_and_b32_e32 v227, 0xffff0000, v243
	v_max_f32_e32 v168, 0x1e3ce508, v168
	v_max_f32_e32 v169, 0x1e3ce508, v169
	v_max_f32_e32 v170, 0x1e3ce508, v170
	v_max_f32_e32 v171, 0x1e3ce508, v171
	v_max_f32_e32 v224, 0x1e3ce508, v224
	v_max_f32_e32 v225, 0x1e3ce508, v225
	v_max_f32_e32 v226, 0x1e3ce508, v226
	v_max_f32_e32 v227, 0x1e3ce508, v227
	v_pk_mul_f32 v[72:73], v[72:73], v[168:169]
	v_pk_mul_f32 v[74:75], v[74:75], v[170:171]
	v_pk_mul_f32 v[68:69], v[68:69], v[224:225]
	v_pk_mul_f32 v[70:71], v[70:71], v[226:227]
	v_cvt_pk_bf16_f32 v240, v72, v73
	v_cvt_pk_bf16_f32 v241, v74, v75
	v_cvt_pk_bf16_f32 v242, v68, v69
	v_cvt_pk_bf16_f32 v243, v70, v71
	v_lshlrev_b32_e32 v168, 16, v244
	v_and_b32_e32 v169, 0xffff0000, v244
	v_lshlrev_b32_e32 v170, 16, v245
	v_and_b32_e32 v171, 0xffff0000, v245
	v_lshlrev_b32_e32 v224, 16, v246
	v_and_b32_e32 v225, 0xffff0000, v246
	v_lshlrev_b32_e32 v226, 16, v247
	v_and_b32_e32 v227, 0xffff0000, v247
	v_max_f32_e32 v168, 0x1e3ce508, v168
	v_max_f32_e32 v169, 0x1e3ce508, v169
	v_max_f32_e32 v170, 0x1e3ce508, v170
	v_max_f32_e32 v171, 0x1e3ce508, v171
	v_max_f32_e32 v224, 0x1e3ce508, v224
	v_max_f32_e32 v225, 0x1e3ce508, v225
	v_max_f32_e32 v226, 0x1e3ce508, v226
	v_max_f32_e32 v227, 0x1e3ce508, v227
	v_pk_mul_f32 v[96:97], v[96:97], v[168:169]
	v_pk_mul_f32 v[98:99], v[98:99], v[170:171]
	v_pk_mul_f32 v[92:93], v[92:93], v[224:225]
	v_pk_mul_f32 v[94:95], v[94:95], v[226:227]
	v_cvt_pk_bf16_f32 v244, v96, v97
	v_cvt_pk_bf16_f32 v245, v98, v99
	v_cvt_pk_bf16_f32 v246, v92, v93
	v_cvt_pk_bf16_f32 v247, v94, v95
	v_lshlrev_b32_e32 v168, 16, v248
	v_and_b32_e32 v169, 0xffff0000, v248
	v_lshlrev_b32_e32 v170, 16, v249
	v_and_b32_e32 v171, 0xffff0000, v249
	v_lshlrev_b32_e32 v224, 16, v250
	v_and_b32_e32 v225, 0xffff0000, v250
	v_lshlrev_b32_e32 v226, 16, v251
	v_and_b32_e32 v227, 0xffff0000, v251
	v_max_f32_e32 v168, 0x1e3ce508, v168
	v_max_f32_e32 v169, 0x1e3ce508, v169
	v_max_f32_e32 v170, 0x1e3ce508, v170
	v_max_f32_e32 v171, 0x1e3ce508, v171
	v_max_f32_e32 v224, 0x1e3ce508, v224
	v_max_f32_e32 v225, 0x1e3ce508, v225
	v_max_f32_e32 v226, 0x1e3ce508, v226
	v_max_f32_e32 v227, 0x1e3ce508, v227
	v_pk_mul_f32 v[64:65], v[64:65], v[168:169]
	v_pk_mul_f32 v[66:67], v[66:67], v[170:171]
	v_pk_mul_f32 v[60:61], v[60:61], v[224:225]
	v_pk_mul_f32 v[62:63], v[62:63], v[226:227]
	v_cvt_pk_bf16_f32 v248, v64, v65
	v_cvt_pk_bf16_f32 v249, v66, v67
	v_cvt_pk_bf16_f32 v250, v60, v61
	v_cvt_pk_bf16_f32 v251, v62, v63
	s_waitcnt vmcnt(9)
	v_lshlrev_b32_e32 v168, 16, v132
	v_and_b32_e32 v169, 0xffff0000, v132
	v_lshlrev_b32_e32 v170, 16, v133
	v_and_b32_e32 v171, 0xffff0000, v133
	v_lshlrev_b32_e32 v224, 16, v134
	v_and_b32_e32 v225, 0xffff0000, v134
	v_lshlrev_b32_e32 v226, 16, v135
	v_and_b32_e32 v227, 0xffff0000, v135
	v_max_f32_e32 v168, 0x1e3ce508, v168
	v_max_f32_e32 v169, 0x1e3ce508, v169
	v_max_f32_e32 v170, 0x1e3ce508, v170
	v_max_f32_e32 v171, 0x1e3ce508, v171
	v_max_f32_e32 v224, 0x1e3ce508, v224
	v_max_f32_e32 v225, 0x1e3ce508, v225
	v_max_f32_e32 v226, 0x1e3ce508, v226
	v_max_f32_e32 v227, 0x1e3ce508, v227
	v_pk_mul_f32 v[88:89], v[88:89], v[168:169]
	v_pk_mul_f32 v[90:91], v[90:91], v[170:171]
	v_pk_mul_f32 v[84:85], v[84:85], v[224:225]
	v_pk_mul_f32 v[86:87], v[86:87], v[226:227]
	v_cvt_pk_bf16_f32 v132, v88, v89
	v_cvt_pk_bf16_f32 v133, v90, v91
	v_cvt_pk_bf16_f32 v134, v84, v85
	v_cvt_pk_bf16_f32 v135, v86, v87
	s_waitcnt vmcnt(8)
	v_lshlrev_b32_e32 v168, 16, v136
	v_and_b32_e32 v169, 0xffff0000, v136
	v_lshlrev_b32_e32 v170, 16, v137
	v_and_b32_e32 v171, 0xffff0000, v137
	v_lshlrev_b32_e32 v224, 16, v138
	v_and_b32_e32 v225, 0xffff0000, v138
	v_lshlrev_b32_e32 v226, 16, v139
	v_and_b32_e32 v227, 0xffff0000, v139
	v_max_f32_e32 v168, 0x1e3ce508, v168
	v_max_f32_e32 v169, 0x1e3ce508, v169
	v_max_f32_e32 v170, 0x1e3ce508, v170
	v_max_f32_e32 v171, 0x1e3ce508, v171
	v_max_f32_e32 v224, 0x1e3ce508, v224
	v_max_f32_e32 v225, 0x1e3ce508, v225
	v_max_f32_e32 v226, 0x1e3ce508, v226
	v_max_f32_e32 v227, 0x1e3ce508, v227
	v_pk_mul_f32 v[56:57], v[56:57], v[168:169]
	v_pk_mul_f32 v[58:59], v[58:59], v[170:171]
	v_pk_mul_f32 v[48:49], v[48:49], v[224:225]
	v_pk_mul_f32 v[50:51], v[50:51], v[226:227]
	v_cvt_pk_bf16_f32 v136, v56, v57
	v_cvt_pk_bf16_f32 v137, v58, v59
	v_cvt_pk_bf16_f32 v138, v48, v49
	v_cvt_pk_bf16_f32 v139, v50, v51
	s_waitcnt vmcnt(7)
	v_lshlrev_b32_e32 v168, 16, v140
	v_and_b32_e32 v169, 0xffff0000, v140
	v_lshlrev_b32_e32 v170, 16, v141
	v_and_b32_e32 v171, 0xffff0000, v141
	v_lshlrev_b32_e32 v224, 16, v142
	v_and_b32_e32 v225, 0xffff0000, v142
	v_lshlrev_b32_e32 v226, 16, v143
	v_and_b32_e32 v227, 0xffff0000, v143
	v_max_f32_e32 v168, 0x1e3ce508, v168
	v_max_f32_e32 v169, 0x1e3ce508, v169
	v_max_f32_e32 v170, 0x1e3ce508, v170
	v_max_f32_e32 v171, 0x1e3ce508, v171
	v_max_f32_e32 v224, 0x1e3ce508, v224
	v_max_f32_e32 v225, 0x1e3ce508, v225
	v_max_f32_e32 v226, 0x1e3ce508, v226
	v_max_f32_e32 v227, 0x1e3ce508, v227
	v_pk_mul_f32 v[52:53], v[52:53], v[168:169]
	v_pk_mul_f32 v[54:55], v[54:55], v[170:171]
	v_pk_mul_f32 v[44:45], v[44:45], v[224:225]
	v_pk_mul_f32 v[46:47], v[46:47], v[226:227]
	v_cvt_pk_bf16_f32 v140, v52, v53
	v_cvt_pk_bf16_f32 v141, v54, v55
	v_cvt_pk_bf16_f32 v142, v44, v45
	v_cvt_pk_bf16_f32 v143, v46, v47
	s_waitcnt vmcnt(6)
	v_lshlrev_b32_e32 v168, 16, v144
	v_and_b32_e32 v169, 0xffff0000, v144
	v_lshlrev_b32_e32 v170, 16, v145
	v_and_b32_e32 v171, 0xffff0000, v145
	v_lshlrev_b32_e32 v224, 16, v146
	v_and_b32_e32 v225, 0xffff0000, v146
	v_lshlrev_b32_e32 v226, 16, v147
	v_and_b32_e32 v227, 0xffff0000, v147
	v_max_f32_e32 v168, 0x1e3ce508, v168
	v_max_f32_e32 v169, 0x1e3ce508, v169
	v_max_f32_e32 v170, 0x1e3ce508, v170
	v_max_f32_e32 v171, 0x1e3ce508, v171
	v_max_f32_e32 v224, 0x1e3ce508, v224
	v_max_f32_e32 v225, 0x1e3ce508, v225
	v_max_f32_e32 v226, 0x1e3ce508, v226
	v_max_f32_e32 v227, 0x1e3ce508, v227
	v_pk_mul_f32 v[16:17], v[16:17], v[168:169]
	v_pk_mul_f32 v[18:19], v[18:19], v[170:171]
	v_pk_mul_f32 v[12:13], v[12:13], v[224:225]
	v_pk_mul_f32 v[14:15], v[14:15], v[226:227]
	v_cvt_pk_bf16_f32 v144, v16, v17
	v_cvt_pk_bf16_f32 v145, v18, v19
	v_cvt_pk_bf16_f32 v146, v12, v13
	v_cvt_pk_bf16_f32 v147, v14, v15
	s_waitcnt vmcnt(5)
	v_lshlrev_b32_e32 v168, 16, v148
	v_and_b32_e32 v169, 0xffff0000, v148
	v_lshlrev_b32_e32 v170, 16, v149
	v_and_b32_e32 v171, 0xffff0000, v149
	v_lshlrev_b32_e32 v224, 16, v150
	v_and_b32_e32 v225, 0xffff0000, v150
	v_lshlrev_b32_e32 v226, 16, v151
	v_and_b32_e32 v227, 0xffff0000, v151
	v_max_f32_e32 v168, 0x1e3ce508, v168
	v_max_f32_e32 v169, 0x1e3ce508, v169
	v_max_f32_e32 v170, 0x1e3ce508, v170
	v_max_f32_e32 v171, 0x1e3ce508, v171
	v_max_f32_e32 v224, 0x1e3ce508, v224
	v_max_f32_e32 v225, 0x1e3ce508, v225
	v_max_f32_e32 v226, 0x1e3ce508, v226
	v_max_f32_e32 v227, 0x1e3ce508, v227
	v_pk_mul_f32 v[40:41], v[40:41], v[168:169]
	v_pk_mul_f32 v[42:43], v[42:43], v[170:171]
	v_pk_mul_f32 v[36:37], v[36:37], v[224:225]
	v_pk_mul_f32 v[38:39], v[38:39], v[226:227]
	v_cvt_pk_bf16_f32 v148, v40, v41
	v_cvt_pk_bf16_f32 v149, v42, v43
	v_cvt_pk_bf16_f32 v150, v36, v37
	v_cvt_pk_bf16_f32 v151, v38, v39
	s_waitcnt vmcnt(4)
	v_lshlrev_b32_e32 v168, 16, v152
	v_and_b32_e32 v169, 0xffff0000, v152
	v_lshlrev_b32_e32 v170, 16, v153
	v_and_b32_e32 v171, 0xffff0000, v153
	v_lshlrev_b32_e32 v224, 16, v154
	v_and_b32_e32 v225, 0xffff0000, v154
	v_lshlrev_b32_e32 v226, 16, v155
	v_and_b32_e32 v227, 0xffff0000, v155
	v_max_f32_e32 v168, 0x1e3ce508, v168
	v_max_f32_e32 v169, 0x1e3ce508, v169
	v_max_f32_e32 v170, 0x1e3ce508, v170
	v_max_f32_e32 v171, 0x1e3ce508, v171
	v_max_f32_e32 v224, 0x1e3ce508, v224
	v_max_f32_e32 v225, 0x1e3ce508, v225
	v_max_f32_e32 v226, 0x1e3ce508, v226
	v_max_f32_e32 v227, 0x1e3ce508, v227
	v_pk_mul_f32 v[8:9], v[8:9], v[168:169]
	v_pk_mul_f32 v[10:11], v[10:11], v[170:171]
	v_pk_mul_f32 v[4:5], v[4:5], v[224:225]
	v_pk_mul_f32 v[6:7], v[6:7], v[226:227]
	v_cvt_pk_bf16_f32 v152, v8, v9
	v_cvt_pk_bf16_f32 v153, v10, v11
	v_cvt_pk_bf16_f32 v154, v4, v5
	v_cvt_pk_bf16_f32 v155, v6, v7
	s_waitcnt vmcnt(3)
	v_lshlrev_b32_e32 v168, 16, v156
	v_and_b32_e32 v169, 0xffff0000, v156
	v_lshlrev_b32_e32 v170, 16, v157
	v_and_b32_e32 v171, 0xffff0000, v157
	v_lshlrev_b32_e32 v224, 16, v158
	v_and_b32_e32 v225, 0xffff0000, v158
	v_lshlrev_b32_e32 v226, 16, v159
	v_and_b32_e32 v227, 0xffff0000, v159
	v_max_f32_e32 v168, 0x1e3ce508, v168
	v_max_f32_e32 v169, 0x1e3ce508, v169
	v_max_f32_e32 v170, 0x1e3ce508, v170
	v_max_f32_e32 v171, 0x1e3ce508, v171
	v_max_f32_e32 v224, 0x1e3ce508, v224
	v_max_f32_e32 v225, 0x1e3ce508, v225
	v_max_f32_e32 v226, 0x1e3ce508, v226
	v_max_f32_e32 v227, 0x1e3ce508, v227
	v_pk_mul_f32 v[32:33], v[32:33], v[168:169]
	v_pk_mul_f32 v[34:35], v[34:35], v[170:171]
	v_pk_mul_f32 v[28:29], v[28:29], v[224:225]
	v_pk_mul_f32 v[30:31], v[30:31], v[226:227]
	v_cvt_pk_bf16_f32 v156, v32, v33
	v_cvt_pk_bf16_f32 v157, v34, v35
	v_cvt_pk_bf16_f32 v158, v28, v29
	v_cvt_pk_bf16_f32 v159, v30, v31
	s_waitcnt vmcnt(2)
	v_lshlrev_b32_e32 v168, 16, v160
	v_and_b32_e32 v169, 0xffff0000, v160
	v_lshlrev_b32_e32 v170, 16, v161
	v_and_b32_e32 v171, 0xffff0000, v161
	v_lshlrev_b32_e32 v224, 16, v162
	v_and_b32_e32 v225, 0xffff0000, v162
	v_lshlrev_b32_e32 v226, 16, v163
	v_and_b32_e32 v227, 0xffff0000, v163
	v_max_f32_e32 v168, 0x1e3ce508, v168
	v_max_f32_e32 v169, 0x1e3ce508, v169
	v_max_f32_e32 v170, 0x1e3ce508, v170
	v_max_f32_e32 v171, 0x1e3ce508, v171
	v_max_f32_e32 v224, 0x1e3ce508, v224
	v_max_f32_e32 v225, 0x1e3ce508, v225
	v_max_f32_e32 v226, 0x1e3ce508, v226
	v_max_f32_e32 v227, 0x1e3ce508, v227
	v_pk_mul_f32 v[116:117], v[116:117], v[168:169]
	v_pk_mul_f32 v[118:119], v[118:119], v[170:171]
	v_pk_mul_f32 v[120:121], v[120:121], v[224:225]
	v_pk_mul_f32 v[122:123], v[122:123], v[226:227]
	v_cvt_pk_bf16_f32 v160, v116, v117
	v_cvt_pk_bf16_f32 v161, v118, v119
	v_cvt_pk_bf16_f32 v162, v120, v121
	v_cvt_pk_bf16_f32 v163, v122, v123
	s_waitcnt vmcnt(1)
	v_lshlrev_b32_e32 v168, 16, v180
	v_and_b32_e32 v169, 0xffff0000, v180
	v_lshlrev_b32_e32 v170, 16, v181
	v_and_b32_e32 v171, 0xffff0000, v181
	v_lshlrev_b32_e32 v224, 16, v182
	v_and_b32_e32 v225, 0xffff0000, v182
	v_lshlrev_b32_e32 v226, 16, v183
	v_and_b32_e32 v227, 0xffff0000, v183
	v_max_f32_e32 v168, 0x1e3ce508, v168
	v_max_f32_e32 v169, 0x1e3ce508, v169
	v_max_f32_e32 v170, 0x1e3ce508, v170
	v_max_f32_e32 v171, 0x1e3ce508, v171
	v_max_f32_e32 v224, 0x1e3ce508, v224
	v_max_f32_e32 v225, 0x1e3ce508, v225
	v_max_f32_e32 v226, 0x1e3ce508, v226
	v_max_f32_e32 v227, 0x1e3ce508, v227
	v_pk_mul_f32 v[24:25], v[24:25], v[168:169]
	v_pk_mul_f32 v[26:27], v[26:27], v[170:171]
	v_pk_mul_f32 v[20:21], v[20:21], v[224:225]
	v_pk_mul_f32 v[22:23], v[22:23], v[226:227]
	v_cvt_pk_bf16_f32 v180, v24, v25
	v_cvt_pk_bf16_f32 v181, v26, v27
	v_cvt_pk_bf16_f32 v182, v20, v21
	v_cvt_pk_bf16_f32 v183, v22, v23
	s_waitcnt vmcnt(0)
	v_lshlrev_b32_e32 v168, 16, v184
	v_and_b32_e32 v169, 0xffff0000, v184
	v_lshlrev_b32_e32 v170, 16, v185
	v_and_b32_e32 v171, 0xffff0000, v185
	v_lshlrev_b32_e32 v224, 16, v186
	v_and_b32_e32 v225, 0xffff0000, v186
	v_lshlrev_b32_e32 v226, 16, v187
	v_and_b32_e32 v227, 0xffff0000, v187
	v_max_f32_e32 v168, 0x1e3ce508, v168
	v_max_f32_e32 v169, 0x1e3ce508, v169
	v_max_f32_e32 v170, 0x1e3ce508, v170
	v_max_f32_e32 v171, 0x1e3ce508, v171
	v_max_f32_e32 v224, 0x1e3ce508, v224
	v_max_f32_e32 v225, 0x1e3ce508, v225
	v_max_f32_e32 v226, 0x1e3ce508, v226
	v_max_f32_e32 v227, 0x1e3ce508, v227
	v_pk_mul_f32 v[124:125], v[124:125], v[168:169]
	v_pk_mul_f32 v[126:127], v[126:127], v[170:171]
	v_pk_mul_f32 v[128:129], v[128:129], v[224:225]
	v_pk_mul_f32 v[130:131], v[130:131], v[226:227]
	v_cvt_pk_bf16_f32 v184, v124, v125
	v_cvt_pk_bf16_f32 v185, v126, v127
	v_cvt_pk_bf16_f32 v186, v128, v129
	v_cvt_pk_bf16_f32 v187, v130, v131
	s_add_u32 s6, s16, 0x0
	s_addc_u32 s7, s17, 0
	global_store_dwordx4 v3, v[228:231], s[6:7]
	s_add_u32 s6, s16, 0x0
	s_addc_u32 s7, s17, 0
	global_store_dwordx4 v3, v[232:235], s[6:7] offset:256
	s_add_u32 s6, s16, 0x8000
	s_addc_u32 s7, s17, 0
	global_store_dwordx4 v3, v[236:239], s[6:7]
	s_add_u32 s6, s16, 0x8000
	s_addc_u32 s7, s17, 0
	global_store_dwordx4 v3, v[240:243], s[6:7] offset:256
	s_add_u32 s6, s16, 0x10000
	s_addc_u32 s7, s17, 0
	global_store_dwordx4 v3, v[244:247], s[6:7]
	s_add_u32 s6, s16, 0x10000
	s_addc_u32 s7, s17, 0
	global_store_dwordx4 v3, v[248:251], s[6:7] offset:256
	s_add_u32 s6, s16, 0x18000
	s_addc_u32 s7, s17, 0
	global_store_dwordx4 v3, v[132:135], s[6:7]
	s_add_u32 s6, s16, 0x18000
	s_addc_u32 s7, s17, 0
	global_store_dwordx4 v3, v[136:139], s[6:7] offset:256
	s_add_u32 s6, s16, 0x40000
	s_addc_u32 s7, s17, 0
	global_store_dwordx4 v3, v[140:143], s[6:7]
	s_add_u32 s6, s16, 0x40000
	s_addc_u32 s7, s17, 0
	global_store_dwordx4 v3, v[144:147], s[6:7] offset:256
	s_add_u32 s6, s16, 0x48000
	s_addc_u32 s7, s17, 0
	global_store_dwordx4 v3, v[148:151], s[6:7]
	s_add_u32 s6, s16, 0x48000
	s_addc_u32 s7, s17, 0
	global_store_dwordx4 v3, v[152:155], s[6:7] offset:256
	s_add_u32 s6, s16, 0x50000
	s_addc_u32 s7, s17, 0
	global_store_dwordx4 v3, v[156:159], s[6:7]
	s_add_u32 s6, s16, 0x50000
	s_addc_u32 s7, s17, 0
	global_store_dwordx4 v3, v[160:163], s[6:7] offset:256
	s_add_u32 s6, s16, 0x58000
	s_addc_u32 s7, s17, 0
	global_store_dwordx4 v3, v[180:183], s[6:7]
	s_add_u32 s6, s16, 0x58000
	s_addc_u32 s7, s17, 0
	global_store_dwordx4 v3, v[184:187], s[6:7] offset:256
.Lmg_done:
.LBB0_1377:
	s_and_b64 vcc, exec, s[2:3]
	s_mov_b64 s[2:3], -1
	s_cbranch_vccnz .LBB0_1203
	s_cmp_lt_i32 s63, 8
	s_cbranch_scc1 .LBB0_1380
	v_mov_b32_e32 v2, v1
	v_mov_b32_e32 v3, v1
	v_mov_b32_e32 v0, v1
	v_mov_b64_e32 v[6:7], v[2:3]
	v_mov_b64_e32 v[10:11], v[2:3]
	v_mov_b64_e32 v[14:15], v[2:3]
	v_mov_b64_e32 v[18:19], v[2:3]
	v_mov_b64_e32 v[22:23], v[2:3]
	v_mov_b64_e32 v[26:27], v[2:3]
	v_mov_b64_e32 v[30:31], v[2:3]
	v_mov_b64_e32 v[34:35], v[2:3]
	v_mov_b64_e32 v[38:39], v[2:3]
	v_mov_b64_e32 v[42:43], v[2:3]
	v_mov_b64_e32 v[46:47], v[2:3]
	v_mov_b64_e32 v[54:55], v[2:3]
	v_mov_b64_e32 v[50:51], v[2:3]
	v_mov_b64_e32 v[58:59], v[2:3]
	v_mov_b64_e32 v[62:63], v[2:3]
	v_mov_b64_e32 v[66:67], v[2:3]
	v_mov_b64_e32 v[70:71], v[2:3]
	v_mov_b64_e32 v[74:75], v[2:3]
	v_mov_b64_e32 v[78:79], v[2:3]
	v_mov_b64_e32 v[82:83], v[2:3]
	v_mov_b64_e32 v[86:87], v[2:3]
	v_mov_b64_e32 v[90:91], v[2:3]
	v_mov_b64_e32 v[94:95], v[2:3]
	v_mov_b64_e32 v[98:99], v[2:3]
	v_mov_b64_e32 v[102:103], v[2:3]
	v_mov_b64_e32 v[106:107], v[2:3]
	v_mov_b64_e32 v[110:111], v[2:3]
	v_mov_b64_e32 v[114:115], v[2:3]
	v_mov_b64_e32 v[118:119], v[2:3]
	v_mov_b64_e32 v[122:123], v[2:3]
	v_mov_b64_e32 v[126:127], v[2:3]
	v_mov_b64_e32 v[130:131], v[2:3]
	v_mov_b64_e32 v[4:5], v[0:1]
	v_mov_b64_e32 v[8:9], v[0:1]
	v_mov_b64_e32 v[12:13], v[0:1]
	v_mov_b64_e32 v[16:17], v[0:1]
	v_mov_b64_e32 v[20:21], v[0:1]
	v_mov_b64_e32 v[24:25], v[0:1]
	v_mov_b64_e32 v[28:29], v[0:1]
	v_mov_b64_e32 v[32:33], v[0:1]
	v_mov_b64_e32 v[36:37], v[0:1]
	v_mov_b64_e32 v[40:41], v[0:1]
	v_mov_b64_e32 v[44:45], v[0:1]
	v_mov_b64_e32 v[52:53], v[0:1]
	v_mov_b64_e32 v[48:49], v[0:1]
	v_mov_b64_e32 v[56:57], v[0:1]
	v_mov_b64_e32 v[60:61], v[0:1]
	v_mov_b64_e32 v[64:65], v[0:1]
	v_mov_b64_e32 v[68:69], v[0:1]
	v_mov_b64_e32 v[72:73], v[0:1]
	v_mov_b64_e32 v[76:77], v[0:1]
	v_mov_b64_e32 v[80:81], v[0:1]
	v_mov_b64_e32 v[84:85], v[0:1]
	v_mov_b64_e32 v[88:89], v[0:1]
	v_mov_b64_e32 v[92:93], v[0:1]
	v_mov_b64_e32 v[96:97], v[0:1]
	v_mov_b64_e32 v[100:101], v[0:1]
	v_mov_b64_e32 v[104:105], v[0:1]
	v_mov_b64_e32 v[108:109], v[0:1]
	v_mov_b64_e32 v[112:113], v[0:1]
	v_mov_b64_e32 v[116:117], v[0:1]
	v_mov_b64_e32 v[120:121], v[0:1]
	v_mov_b64_e32 v[124:125], v[0:1]
	v_mov_b64_e32 v[128:129], v[0:1]
